# baseline (speedup 1.0000x reference)
.LE_loop12:
	s_sub_u32 s71, s33, 1
	s_add_u32 s61, s33, 1
	s_min_u32 s61, s61, s60
	s_and_b32 s64, s71, 1
	s_lshl_b32 s64, s64, 22
	s_add_u32 s64, s64, s50
	s_add_u32 s64, s64, 0x60000
	s_add_u32 s36, s6, s64
	s_addc_u32 s37, s7, 0
	s_lshl_b32 s64, s71, 3
	s_add_u32 s64, s64, s29
	s_lshl_b32 s64, s64, 5
	s_add_u32 s64, s64, s30
	s_lshl_b32 s64, s64, 2
	s_add_u32 s40, s8, s64
	s_addc_u32 s41, s9, 0
	s_lshl_b32 s64, s33, 11
	s_lshl_b32 s65, s29, 8
	s_add_u32 s64, s64, s65
	s_add_u32 s64, s64, 128
	s_lshl_b32 s64, s64, 3
	s_add_u32 s42, s12, s64
	s_addc_u32 s43, s13, 0
	s_nop 3
	global_load_dword v228, v249, s[42:43] offset:0
	global_load_dword v229, v249, s[42:43] offset:256
	s_waitcnt lgkmcnt(2)
	v_mfma_f32_32x32x16_f16 v[0:15], a[0:3], v[160:163], v[0:15]
	ds_read_b128 v[160:163], v192 offset:8192
	v_exp_f32_e32 v200, v96
	v_mfma_f32_32x32x16_f16 v[16:31], a[0:3], v[164:167], v[16:31]
	ds_read_b128 v[164:167], v192 offset:9216
	s_lshl_b32 s64, s71, 3
	s_add_u32 s64, s64, s29
	s_lshl_b32 s64, s64, 7
	s_add_u32 s38, s8, s64
	s_addc_u32 s39, s9, 0
	global_load_dword v251, v196, s[38:39] sc1
	v_exp_f32_e32 v201, v97
	v_add_f32_e32 v200, 1.0, v200
	v_mfma_f32_32x32x16_f16 v[0:15], a[4:7], v[168:171], v[0:15]
	ds_read_b128 v[168:171], v192 offset:10240
	v_exp_f32_e32 v202, v98
	v_add_f32_e32 v201, 1.0, v201
	v_mfma_f32_32x32x16_f16 v[16:31], a[4:7], v[172:175], v[16:31]
	ds_read_b128 v[172:175], v192 offset:11264
	global_load_lds_dwordx4 v192, s[44:45] offset:1024 sc1
	v_exp_f32_e32 v203, v99
	v_add_f32_e32 v202, 1.0, v202
	v_mfma_f32_32x32x16_f16 v[0:15], a[8:11], v[176:179], v[0:15]
	ds_read_b128 v[176:179], v192 offset:12288
	v_exp_f32_e32 v204, v100
	v_add_f32_e32 v203, 1.0, v203
	v_mfma_f32_32x32x16_f16 v[16:31], a[8:11], v[180:183], v[16:31]
	ds_read_b128 v[180:183], v192 offset:13312
	v_exp_f32_e32 v205, v101
	v_add_f32_e32 v204, 1.0, v204
	s_waitcnt lgkmcnt(2)
	v_mfma_f32_32x32x16_f16 v[0:15], a[12:15], v[184:187], v[0:15]
	ds_read_b128 v[184:187], v192 offset:14336
	v_exp_f32_e32 v206, v102
	v_add_f32_e32 v205, 1.0, v205
	v_mfma_f32_32x32x16_f16 v[16:31], a[12:15], v[188:191], v[16:31]
	ds_read_b128 v[188:191], v192 offset:15360
	global_load_lds_dwordx4 v192, s[44:45] offset:2048 sc1
	v_exp_f32_e32 v207, v103
	v_add_f32_e32 v206, 1.0, v206
	v_mfma_f32_32x32x16_f16 v[0:15], a[16:19], v[160:163], v[0:15]
	ds_read_b128 v[160:163], v192 offset:16384
	v_exp_f32_e32 v208, v104
	v_add_f32_e32 v207, 1.0, v207
	v_mfma_f32_32x32x16_f16 v[16:31], a[16:19], v[164:167], v[16:31]
	ds_read_b128 v[164:167], v192 offset:17408
	v_exp_f32_e32 v209, v105
	v_add_f32_e32 v208, 1.0, v208
	v_mfma_f32_32x32x16_f16 v[0:15], a[20:23], v[168:171], v[0:15]
	ds_read_b128 v[168:171], v192 offset:18432
	v_exp_f32_e32 v210, v106
	v_add_f32_e32 v209, 1.0, v209
	v_mfma_f32_32x32x16_f16 v[16:31], a[20:23], v[172:175], v[16:31]
	ds_read_b128 v[172:175], v192 offset:19456
	global_load_lds_dwordx4 v192, s[44:45] offset:3072 sc1
	v_exp_f32_e32 v211, v107
	v_add_f32_e32 v210, 1.0, v210
	s_waitcnt lgkmcnt(2)
	v_mfma_f32_32x32x16_f16 v[0:15], a[24:27], v[176:179], v[0:15]
	ds_read_b128 v[176:179], v192 offset:20480
	v_exp_f32_e32 v212, v108
	v_add_f32_e32 v211, 1.0, v211
	v_mfma_f32_32x32x16_f16 v[16:31], a[24:27], v[180:183], v[16:31]
	ds_read_b128 v[180:183], v192 offset:21504
	v_exp_f32_e32 v213, v109
	v_add_f32_e32 v212, 1.0, v212
	v_mfma_f32_32x32x16_f16 v[0:15], a[28:31], v[184:187], v[0:15]
	ds_read_b128 v[184:187], v192 offset:22528
	v_exp_f32_e32 v214, v110
	v_add_f32_e32 v213, 1.0, v213
	v_mfma_f32_32x32x16_f16 v[16:31], a[28:31], v[188:191], v[16:31]
	ds_read_b128 v[188:191], v192 offset:23552
	s_mov_b32 m0, s57
	s_add_u32 s44, s34, 0x11000
	s_addc_u32 s45, s35, 0
	global_load_lds_dwordx4 v192, s[44:45] sc1
	v_exp_f32_e32 v215, v111
	v_add_f32_e32 v214, 1.0, v214
	v_mfma_f32_32x32x16_f16 v[0:15], a[32:35], v[160:163], v[0:15]
	ds_read_b128 v[160:163], v192 offset:24576
	v_add_f32_e32 v215, 1.0, v215
	v_rcp_f32_e32 v200, v200
	v_mfma_f32_32x32x16_f16 v[16:31], a[32:35], v[164:167], v[16:31]
	ds_read_b128 v[164:167], v192 offset:25600
	v_rcp_f32_e32 v201, v201
	s_waitcnt lgkmcnt(2)
	v_mfma_f32_32x32x16_f16 v[0:15], a[36:39], v[168:171], v[0:15]
	ds_read_b128 v[168:171], v192 offset:26624
	v_rcp_f32_e32 v202, v202
	v_mfma_f32_32x32x16_f16 v[16:31], a[36:39], v[172:175], v[16:31]
	ds_read_b128 v[172:175], v192 offset:27648
	global_load_lds_dwordx4 v192, s[44:45] offset:1024 sc1
	v_rcp_f32_e32 v203, v203
	v_mfma_f32_32x32x16_f16 v[0:15], a[40:43], v[176:179], v[0:15]
	ds_read_b128 v[176:179], v192 offset:28672
	v_rcp_f32_e32 v204, v204
	v_mfma_f32_32x32x16_f16 v[16:31], a[40:43], v[180:183], v[16:31]
	ds_read_b128 v[180:183], v192 offset:29696
	v_rcp_f32_e32 v205, v205
	v_mul_f32_e32 v204, v204, v152
	v_mfma_f32_32x32x16_f16 v[0:15], a[44:47], v[184:187], v[0:15]
	ds_read_b128 v[184:187], v192 offset:30720
	v_rcp_f32_e32 v206, v206
	v_mul_f32_e32 v205, v205, v153
	v_mfma_f32_32x32x16_f16 v[16:31], a[44:47], v[188:191], v[16:31]
	ds_read_b128 v[188:191], v192 offset:31744
	global_load_lds_dwordx4 v192, s[44:45] offset:2048 sc1
	v_rcp_f32_e32 v207, v207
	v_mul_f32_e32 v206, v206, v154
	s_waitcnt vmcnt(10)
	s_barrier
	s_waitcnt lgkmcnt(2)
	v_mfma_f32_32x32x16_f16 v[0:15], a[48:51], v[160:163], v[0:15]
	ds_read_b128 v[160:163], v192 offset:32768
	v_rcp_f32_e32 v208, v208
	v_mul_f32_e32 v207, v207, v155
	v_mfma_f32_32x32x16_f16 v[16:31], a[48:51], v[164:167], v[16:31]
	ds_read_b128 v[164:167], v192 offset:33792
	v_rcp_f32_e32 v209, v209
	v_fmamk_f32 v208, v208, 0xc0b8aa3b, v198
	v_mfma_f32_32x32x16_f16 v[0:15], a[52:55], v[168:171], v[0:15]
	ds_read_b128 v[168:171], v192 offset:34816
	v_rcp_f32_e32 v210, v210
	v_fmamk_f32 v209, v209, 0xc0b8aa3b, v198
	v_fma_f32 v152, v200, v208, v204
	v_mfma_f32_32x32x16_f16 v[16:31], a[52:55], v[172:175], v[16:31]
	ds_read_b128 v[172:175], v192 offset:35840
	global_load_lds_dwordx4 v192, s[44:45] offset:3072 sc1
	v_rcp_f32_e32 v211, v211
	v_fmamk_f32 v210, v210, 0xc0b8aa3b, v198
	v_fma_f32 v153, v201, v209, v205
	v_mfma_f32_32x32x16_f16 v[0:15], a[56:59], v[176:179], v[0:15]
	ds_read_b128 v[176:179], v192 offset:36864
	v_rcp_f32_e32 v212, v212
	v_fmamk_f32 v211, v211, 0xc0b8aa3b, v198
	v_fma_f32 v154, v202, v210, v206
	v_mfma_f32_32x32x16_f16 v[16:31], a[56:59], v[180:183], v[16:31]
	ds_read_b128 v[180:183], v192 offset:37888
	v_rcp_f32_e32 v213, v213
	v_fma_f32 v155, v203, v211, v207
	s_waitcnt lgkmcnt(2)
	v_mfma_f32_32x32x16_f16 v[0:15], a[60:63], v[184:187], v[0:15]
	ds_read_b128 v[184:187], v192 offset:38912
	v_rcp_f32_e32 v214, v214
	v_mfma_f32_32x32x16_f16 v[16:31], a[60:63], v[188:191], v[16:31]
	ds_read_b128 v[188:191], v192 offset:39936
	s_mov_b32 m0, s58
	s_add_u32 s44, s34, 0x18000
	s_addc_u32 s45, s35, 0
	global_load_lds_dwordx4 v192, s[44:45] sc1
	v_rcp_f32_e32 v215, v215
	v_mfma_f32_32x32x16_f16 v[0:15], a[64:67], v[160:163], v[0:15]
	ds_read_b128 v[160:163], v192 offset:40960
	v_exp_f32_e32 v200, v152
	v_mfma_f32_32x32x16_f16 v[16:31], a[64:67], v[164:167], v[16:31]
	ds_read_b128 v[164:167], v192 offset:41984
	v_exp_f32_e32 v201, v153
	v_add_f32_e32 v200, 1.0, v200
	v_mfma_f32_32x32x16_f16 v[0:15], a[68:71], v[168:171], v[0:15]
	ds_read_b128 v[168:171], v192 offset:43008
	v_exp_f32_e32 v202, v154
	v_add_f32_e32 v201, 1.0, v201
	v_mfma_f32_32x32x16_f16 v[16:31], a[68:71], v[172:175], v[16:31]
	ds_read_b128 v[172:175], v192 offset:44032
	global_load_lds_dwordx4 v192, s[44:45] offset:1024 sc1
	v_exp_f32_e32 v203, v155
	v_add_f32_e32 v202, 1.0, v202
	s_waitcnt lgkmcnt(2)
	v_mfma_f32_32x32x16_f16 v[0:15], a[72:75], v[176:179], v[0:15]
	ds_read_b128 v[176:179], v192 offset:45056
	v_add_f32_e32 v203, 1.0, v203
	v_rcp_f32_e32 v200, v200
	v_mfma_f32_32x32x16_f16 v[16:31], a[72:75], v[180:183], v[16:31]
	ds_read_b128 v[180:183], v192 offset:46080
	v_rcp_f32_e32 v201, v201
	v_fma_f32 v200, v200, 2.0, -1.0
	v_mfma_f32_32x32x16_f16 v[0:15], a[76:79], v[184:187], v[0:15]
	ds_read_b128 v[184:187], v192 offset:47104
	v_rcp_f32_e32 v202, v202
	v_fma_f32 v201, v201, 2.0, -1.0
	v_mul_f32_e32 v216, v212, v200
	v_mfma_f32_32x32x16_f16 v[16:31], a[76:79], v[188:191], v[16:31]
	ds_read_b128 v[188:191], v192 offset:48128
	global_load_lds_dwordx4 v192, s[44:45] offset:2048 sc1
	v_rcp_f32_e32 v203, v203
	v_fma_f32 v202, v202, 2.0, -1.0
	v_mul_f32_e32 v217, v213, v201
	v_mfma_f32_32x32x16_f16 v[0:15], a[80:83], v[160:163], v[0:15]
	ds_read_b128 v[160:163], v192 offset:49152
	v_fma_f32 v203, v203, 2.0, -1.0
	v_mul_f32_e32 v218, v214, v202
	v_exp_f32_e32 v200, v112
	v_mfma_f32_32x32x16_f16 v[16:31], a[80:83], v[164:167], v[16:31]
	ds_read_b128 v[164:167], v192 offset:50176
	v_mul_f32_e32 v219, v215, v203
	v_cvt_pk_f16_f32 v220, v216, v217
	v_exp_f32_e32 v201, v113
	s_waitcnt lgkmcnt(2)
	v_mfma_f32_32x32x16_f16 v[0:15], a[84:87], v[168:171], v[0:15]
	ds_read_b128 v[168:171], v192 offset:51200
	v_cvt_pk_f16_f32 v221, v218, v219
	v_exp_f32_e32 v202, v114
	v_add_f32_e32 v200, 1.0, v200
	v_mfma_f32_32x32x16_f16 v[16:31], a[84:87], v[172:175], v[16:31]
	ds_read_b128 v[172:175], v192 offset:52224
	global_load_lds_dwordx4 v192, s[44:45] offset:3072 sc1
	v_exp_f32_e32 v203, v115
	v_add_f32_e32 v201, 1.0, v201
	v_add_f32_e32 v202, 1.0, v202
	v_mfma_f32_32x32x16_f16 v[0:15], a[88:91], v[176:179], v[0:15]
	ds_read_b128 v[176:179], v192 offset:53248
	v_exp_f32_e32 v204, v116
	v_add_f32_e32 v203, 1.0, v203
	v_mfma_f32_32x32x16_f16 v[16:31], a[88:91], v[180:183], v[16:31]
	ds_read_b128 v[180:183], v192 offset:54272
	v_exp_f32_e32 v205, v117
	v_add_f32_e32 v204, 1.0, v204
	v_mfma_f32_32x32x16_f16 v[0:15], a[92:95], v[184:187], v[0:15]
	ds_read_b128 v[184:187], v192 offset:55296
	v_exp_f32_e32 v206, v118
	v_add_f32_e32 v205, 1.0, v205
	v_mfma_f32_32x32x16_f16 v[16:31], a[92:95], v[188:191], v[16:31]
	ds_read_b128 v[188:191], v192 offset:56320
	s_mov_b32 m0, s59
	s_add_u32 s44, s34, 0x19000
	s_addc_u32 s45, s35, 0
	global_load_lds_dwordx4 v192, s[44:45] sc1
	v_exp_f32_e32 v207, v119
	v_add_f32_e32 v206, 1.0, v206
	s_waitcnt lgkmcnt(2)
	v_mfma_f32_32x32x16_f16 v[0:15], a[96:99], v[160:163], v[0:15]
	ds_read_b128 v[160:163], v192 offset:57344
	v_exp_f32_e32 v208, v120
	v_add_f32_e32 v207, 1.0, v207
	v_mfma_f32_32x32x16_f16 v[16:31], a[96:99], v[164:167], v[16:31]
	ds_read_b128 v[164:167], v192 offset:58368
	v_exp_f32_e32 v209, v121
	v_add_f32_e32 v208, 1.0, v208
	v_mfma_f32_32x32x16_f16 v[0:15], a[100:103], v[168:171], v[0:15]
	ds_read_b128 v[168:171], v192 offset:59392
	v_exp_f32_e32 v210, v122
	v_add_f32_e32 v209, 1.0, v209
	v_mfma_f32_32x32x16_f16 v[16:31], a[100:103], v[172:175], v[16:31]
	ds_read_b128 v[172:175], v192 offset:60416
	global_load_lds_dwordx4 v192, s[44:45] offset:1024 sc1
	v_exp_f32_e32 v211, v123
	v_add_f32_e32 v210, 1.0, v210
	v_mfma_f32_32x32x16_f16 v[0:15], a[104:107], v[176:179], v[0:15]
	ds_read_b128 v[176:179], v192 offset:61440
	v_exp_f32_e32 v212, v124
	v_add_f32_e32 v211, 1.0, v211
	v_mfma_f32_32x32x16_f16 v[16:31], a[104:107], v[180:183], v[16:31]
	ds_read_b128 v[180:183], v192 offset:62464
	v_exp_f32_e32 v213, v125
	v_add_f32_e32 v212, 1.0, v212
	s_waitcnt lgkmcnt(2)
	v_mfma_f32_32x32x16_f16 v[0:15], a[108:111], v[184:187], v[0:15]
	ds_read_b128 v[184:187], v192 offset:63488
	v_exp_f32_e32 v214, v126
	v_add_f32_e32 v213, 1.0, v213
	v_mfma_f32_32x32x16_f16 v[16:31], a[108:111], v[188:191], v[16:31]
	ds_read_b128 v[188:191], v192 offset:64512
	global_load_lds_dwordx4 v192, s[44:45] offset:2048 sc1
	v_exp_f32_e32 v215, v127
	v_add_f32_e32 v214, 1.0, v214
	s_waitcnt vmcnt(7)
	s_barrier
	v_mfma_f32_32x32x16_f16 v[0:15], a[112:115], v[160:163], v[0:15]
	ds_read_b128 v[160:163], v193 offset:0
	v_add_f32_e32 v215, 1.0, v215
	v_rcp_f32_e32 v200, v200
	v_mfma_f32_32x32x16_f16 v[16:31], a[112:115], v[164:167], v[16:31]
	ds_read_b128 v[164:167], v193 offset:1024
	v_rcp_f32_e32 v201, v201
	v_mfma_f32_32x32x16_f16 v[0:15], a[116:119], v[168:171], v[0:15]
	ds_read_b128 v[168:171], v193 offset:2048
	v_rcp_f32_e32 v202, v202
	v_mfma_f32_32x32x16_f16 v[16:31], a[116:119], v[172:175], v[16:31]
	ds_read_b128 v[172:175], v193 offset:3072
	global_load_lds_dwordx4 v192, s[44:45] offset:3072 sc1
	v_rcp_f32_e32 v203, v203
	s_waitcnt lgkmcnt(2)
	v_mfma_f32_32x32x16_f16 v[0:15], a[120:123], v[176:179], v[0:15]
	ds_read_b128 v[176:179], v193 offset:4096
	v_rcp_f32_e32 v204, v204
	v_mfma_f32_32x32x16_f16 v[16:31], a[120:123], v[180:183], v[16:31]
	ds_read_b128 v[180:183], v193 offset:5120
	v_rcp_f32_e32 v205, v205
	v_mul_f32_e32 v204, v204, v156
	v_mfma_f32_32x32x16_f16 v[0:15], a[124:127], v[184:187], v[0:15]
	ds_read_b128 v[184:187], v193 offset:6144
	v_rcp_f32_e32 v206, v206
	v_mul_f32_e32 v205, v205, v157
	v_mfma_f32_32x32x16_f16 v[16:31], a[124:127], v[188:191], v[16:31]
	ds_read_b128 v[188:191], v193 offset:7168
	v_cmp_gt_u32_e32 vcc, 2, v251
	s_cbranch_vccnz .LE_tpoll17
.LE_tok16:
	s_and_b32 s64, s71, 1
	s_lshl_b32 s64, s64, 22
	s_add_u32 s64, s64, s49
	s_add_u32 s64, s64, 0x20000
	s_add_u32 s34, s6, s64
	s_addc_u32 s35, s7, 0
	s_mov_b32 m0, s52
	s_add_u32 s44, s34, 0x0
	s_addc_u32 s45, s35, 0
	global_load_lds_dwordx4 v192, s[44:45] sc1
	v_rcp_f32_e32 v207, v207
	v_mul_f32_e32 v206, v206, v158
	v_mfma_f32_32x32x16_f16 v[0:15], a[128:131], v[160:163], v[0:15]
	ds_read_b128 v[160:163], v193 offset:8192
	v_rcp_f32_e32 v208, v208
	v_mul_f32_e32 v207, v207, v159
	v_mfma_f32_32x32x16_f16 v[16:31], a[128:131], v[164:167], v[16:31]
	ds_read_b128 v[164:167], v193 offset:9216
	v_rcp_f32_e32 v209, v209
	v_fmamk_f32 v208, v208, 0xc0b8aa3b, v198
	s_waitcnt lgkmcnt(2)
	v_mfma_f32_32x32x16_f16 v[0:15], a[132:135], v[168:171], v[0:15]
	ds_read_b128 v[168:171], v193 offset:10240
	v_rcp_f32_e32 v210, v210
	v_fmamk_f32 v209, v209, 0xc0b8aa3b, v198
	v_fma_f32 v156, v200, v208, v204
	v_mfma_f32_32x32x16_f16 v[16:31], a[132:135], v[172:175], v[16:31]
	ds_read_b128 v[172:175], v193 offset:11264
	global_load_lds_dwordx4 v192, s[44:45] offset:1024 sc1
	v_rcp_f32_e32 v211, v211
	v_fmamk_f32 v210, v210, 0xc0b8aa3b, v198
	v_fma_f32 v157, v201, v209, v205
	v_mfma_f32_32x32x2_f32 v[64:79], v248, v228, v[232:247]
	v_mfma_f32_32x32x16_f16 v[0:15], a[136:139], v[176:179], v[0:15]
	ds_read_b128 v[176:179], v193 offset:12288
	v_rcp_f32_e32 v212, v212
	v_fmamk_f32 v211, v211, 0xc0b8aa3b, v198
	v_fma_f32 v158, v202, v210, v206
	v_mfma_f32_32x32x2_f32 v[80:95], v248, v229, v[232:247]
	v_mfma_f32_32x32x16_f16 v[16:31], a[136:139], v[180:183], v[16:31]
	ds_read_b128 v[180:183], v193 offset:13312
	v_rcp_f32_e32 v213, v213
	v_fma_f32 v159, v203, v211, v207
	v_mfma_f32_32x32x16_f16 v[0:15], a[140:143], v[184:187], v[0:15]
	ds_read_b128 v[184:187], v193 offset:14336
	v_rcp_f32_e32 v214, v214
	v_mfma_f32_32x32x16_f16 v[16:31], a[140:143], v[188:191], v[16:31]
	ds_read_b128 v[188:191], v193 offset:15360
	global_load_lds_dwordx4 v192, s[44:45] offset:2048 sc1
	v_rcp_f32_e32 v215, v215
	s_waitcnt lgkmcnt(2)
	v_mfma_f32_32x32x16_f16 v[0:15], a[144:147], v[160:163], v[0:15]
	ds_read_b128 v[160:163], v193 offset:16384
	v_exp_f32_e32 v200, v156
	v_mfma_f32_32x32x16_f16 v[16:31], a[144:147], v[164:167], v[16:31]
	ds_read_b128 v[164:167], v193 offset:17408
	v_exp_f32_e32 v201, v157
	v_add_f32_e32 v200, 1.0, v200
	v_mfma_f32_32x32x16_f16 v[0:15], a[148:151], v[168:171], v[0:15]
	ds_read_b128 v[168:171], v193 offset:18432
	v_exp_f32_e32 v202, v158
	v_add_f32_e32 v201, 1.0, v201
	v_mfma_f32_32x32x16_f16 v[16:31], a[148:151], v[172:175], v[16:31]
	ds_read_b128 v[172:175], v193 offset:19456
	global_load_lds_dwordx4 v192, s[44:45] offset:3072 sc1
	v_exp_f32_e32 v203, v159
	v_add_f32_e32 v202, 1.0, v202
	v_mfma_f32_32x32x16_f16 v[0:15], a[152:155], v[176:179], v[0:15]
	ds_read_b128 v[176:179], v193 offset:20480
	v_add_f32_e32 v203, 1.0, v203
	v_rcp_f32_e32 v200, v200
	v_mfma_f32_32x32x16_f16 v[16:31], a[152:155], v[180:183], v[16:31]
	ds_read_b128 v[180:183], v193 offset:21504
	v_rcp_f32_e32 v201, v201
	v_fma_f32 v200, v200, 2.0, -1.0
	s_waitcnt lgkmcnt(2)
	v_mfma_f32_32x32x16_f16 v[0:15], a[156:159], v[184:187], v[0:15]
	ds_read_b128 v[184:187], v193 offset:22528
	v_rcp_f32_e32 v202, v202
	v_fma_f32 v201, v201, 2.0, -1.0
	v_mul_f32_e32 v216, v212, v200
	v_mfma_f32_32x32x16_f16 v[16:31], a[156:159], v[188:191], v[16:31]
	ds_read_b128 v[188:191], v193 offset:23552
	s_mov_b32 m0, s53
	s_add_u32 s44, s34, 0x1000
	s_addc_u32 s45, s35, 0
	global_load_lds_dwordx4 v192, s[44:45] sc1
	v_rcp_f32_e32 v203, v203
	v_fma_f32 v202, v202, 2.0, -1.0
	v_mul_f32_e32 v217, v213, v201
	v_mfma_f32_32x32x16_f16 v[0:15], a[160:163], v[160:163], v[0:15]
	ds_read_b128 v[160:163], v193 offset:24576
	v_fma_f32 v203, v203, 2.0, -1.0
	v_mul_f32_e32 v218, v214, v202
	v_mfma_f32_32x32x16_f16 v[16:31], a[160:163], v[164:167], v[16:31]
	ds_read_b128 v[164:167], v193 offset:25600
	v_mul_f32_e32 v219, v215, v203
	v_cvt_pk_f16_f32 v222, v216, v217
	v_mfma_f32_32x32x16_f16 v[0:15], a[164:167], v[168:171], v[0:15]
	ds_read_b128 v[168:171], v193 offset:26624
	v_cvt_pk_f16_f32 v223, v218, v219
	v_mfma_f32_32x32x16_f16 v[16:31], a[164:167], v[172:175], v[16:31]
	ds_read_b128 v[172:175], v193 offset:27648
	global_load_lds_dwordx4 v192, s[44:45] offset:1024 sc1
	v_permlane32_swap_b32_e32 v220, v222
	v_permlane32_swap_b32_e32 v221, v223
	s_cmp_eq_u32 s31, 0
	s_cbranch_scc1 .LE_slow18
	global_store_dwordx4 v195, v[220:223], s[36:37] offset:0

.LE_htb23:
	v_exp_f32_e32 v203, v19
	v_mfma_f32_32x32x16_f16 v[32:47], a[88:91], v[176:179], v[32:47]
	ds_read_b128 v[176:179], v192 offset:53248
	v_exp_f32_e32 v204, v20
	v_add_f32_e32 v201, 1.0, v201
	v_add_f32_e32 v202, 1.0, v202
	v_mfma_f32_32x32x16_f16 v[48:63], a[88:91], v[180:183], v[48:63]
	ds_read_b128 v[180:183], v192 offset:54272
	v_exp_f32_e32 v205, v21
	v_add_f32_e32 v203, 1.0, v203
	v_add_f32_e32 v204, 1.0, v204
	v_mfma_f32_32x32x16_f16 v[32:47], a[92:95], v[184:187], v[32:47]
	ds_read_b128 v[184:187], v192 offset:55296
	v_exp_f32_e32 v206, v22
	v_add_f32_e32 v205, 1.0, v205
	v_mfma_f32_32x32x16_f16 v[48:63], a[92:95], v[188:191], v[48:63]
	ds_read_b128 v[188:191], v192 offset:56320
	s_mov_b32 m0, s59
	s_add_u32 s44, s34, 0x19000
	s_addc_u32 s45, s35, 0
	global_load_lds_dwordx4 v192, s[44:45] sc1
	v_exp_f32_e32 v207, v23
	v_add_f32_e32 v206, 1.0, v206
	s_waitcnt lgkmcnt(2)
	v_mfma_f32_32x32x16_f16 v[32:47], a[96:99], v[160:163], v[32:47]
	ds_read_b128 v[160:163], v192 offset:57344
	v_exp_f32_e32 v208, v24
	v_add_f32_e32 v207, 1.0, v207
	v_mfma_f32_32x32x16_f16 v[48:63], a[96:99], v[164:167], v[48:63]
	ds_read_b128 v[164:167], v192 offset:58368
	v_exp_f32_e32 v209, v25
	v_add_f32_e32 v208, 1.0, v208
	v_mfma_f32_32x32x16_f16 v[32:47], a[100:103], v[168:171], v[32:47]
	ds_read_b128 v[168:171], v192 offset:59392
	v_exp_f32_e32 v210, v26
	v_add_f32_e32 v209, 1.0, v209
	v_mfma_f32_32x32x16_f16 v[48:63], a[100:103], v[172:175], v[48:63]
	ds_read_b128 v[172:175], v192 offset:60416
	global_load_lds_dwordx4 v192, s[44:45] offset:1024 sc1
	v_exp_f32_e32 v211, v27
	v_add_f32_e32 v210, 1.0, v210
	v_mfma_f32_32x32x16_f16 v[32:47], a[104:107], v[176:179], v[32:47]
	ds_read_b128 v[176:179], v192 offset:61440
	v_exp_f32_e32 v212, v28
	v_add_f32_e32 v211, 1.0, v211
	v_mfma_f32_32x32x16_f16 v[48:63], a[104:107], v[180:183], v[48:63]
	ds_read_b128 v[180:183], v192 offset:62464
	v_exp_f32_e32 v213, v29
	v_add_f32_e32 v212, 1.0, v212
	s_waitcnt lgkmcnt(2)
	v_mfma_f32_32x32x16_f16 v[32:47], a[108:111], v[184:187], v[32:47]
	ds_read_b128 v[184:187], v192 offset:63488
	v_exp_f32_e32 v214, v30
	v_add_f32_e32 v213, 1.0, v213
	v_mfma_f32_32x32x16_f16 v[48:63], a[108:111], v[188:191], v[48:63]
	ds_read_b128 v[188:191], v192 offset:64512
	global_load_lds_dwordx4 v192, s[44:45] offset:2048 sc1
	v_exp_f32_e32 v215, v31
	v_add_f32_e32 v214, 1.0, v214
	s_waitcnt vmcnt(7)
	s_barrier
	v_mfma_f32_32x32x16_f16 v[32:47], a[112:115], v[160:163], v[32:47]
	ds_read_b128 v[160:163], v193 offset:0
	v_add_f32_e32 v215, 1.0, v215
	v_rcp_f32_e32 v200, v200
	v_mfma_f32_32x32x16_f16 v[48:63], a[112:115], v[164:167], v[48:63]
	ds_read_b128 v[164:167], v193 offset:1024
	v_rcp_f32_e32 v201, v201
	v_mfma_f32_32x32x16_f16 v[32:47], a[116:119], v[168:171], v[32:47]
	ds_read_b128 v[168:171], v193 offset:2048
	v_rcp_f32_e32 v202, v202
	v_mfma_f32_32x32x16_f16 v[48:63], a[116:119], v[172:175], v[48:63]
	ds_read_b128 v[172:175], v193 offset:3072
	global_load_lds_dwordx4 v192, s[44:45] offset:3072 sc1
	v_rcp_f32_e32 v203, v203
	s_waitcnt lgkmcnt(2)
	v_mfma_f32_32x32x16_f16 v[32:47], a[120:123], v[176:179], v[32:47]
	ds_read_b128 v[176:179], v193 offset:4096
	v_rcp_f32_e32 v204, v204
	v_mfma_f32_32x32x16_f16 v[48:63], a[120:123], v[180:183], v[48:63]
	ds_read_b128 v[180:183], v193 offset:5120
	v_rcp_f32_e32 v205, v205
	v_mul_f32_e32 v204, v204, v132
	v_mfma_f32_32x32x16_f16 v[32:47], a[124:127], v[184:187], v[32:47]
	ds_read_b128 v[184:187], v193 offset:6144
	v_rcp_f32_e32 v206, v206
	v_mul_f32_e32 v205, v205, v133
	v_mfma_f32_32x32x16_f16 v[48:63], a[124:127], v[188:191], v[48:63]
	ds_read_b128 v[188:191], v193 offset:7168
	v_cmp_gt_u32_e32 vcc, 3, v251
	s_cbranch_vccnz .LE_tpoll25
.LE_tok24:
	s_and_b32 s64, s71, 1
	s_lshl_b32 s64, s64, 22
	s_add_u32 s64, s64, s49
	s_add_u32 s64, s64, 0x40000
	s_add_u32 s34, s6, s64
	s_addc_u32 s35, s7, 0
	s_mov_b32 m0, s52
	s_add_u32 s44, s34, 0x0
	s_addc_u32 s45, s35, 0
	global_load_lds_dwordx4 v192, s[44:45] sc1
	v_rcp_f32_e32 v207, v207
	v_mul_f32_e32 v206, v206, v134
	v_mfma_f32_32x32x16_f16 v[32:47], a[128:131], v[160:163], v[32:47]
	ds_read_b128 v[160:163], v193 offset:8192
	v_rcp_f32_e32 v208, v208
	v_mul_f32_e32 v207, v207, v135
	v_mfma_f32_32x32x16_f16 v[48:63], a[128:131], v[164:167], v[48:63]
	ds_read_b128 v[164:167], v193 offset:9216
	v_rcp_f32_e32 v209, v209
	v_fmamk_f32 v208, v208, 0xc0b8aa3b, v198
	s_waitcnt lgkmcnt(2)
	v_mfma_f32_32x32x16_f16 v[32:47], a[132:135], v[168:171], v[32:47]
	ds_read_b128 v[168:171], v193 offset:10240
	v_rcp_f32_e32 v210, v210
	v_fmamk_f32 v209, v209, 0xc0b8aa3b, v198
	v_fma_f32 v132, v200, v208, v204
	v_mfma_f32_32x32x16_f16 v[48:63], a[132:135], v[172:175], v[48:63]
	ds_read_b128 v[172:175], v193 offset:11264
	global_load_lds_dwordx4 v192, s[44:45] offset:1024 sc1
	v_rcp_f32_e32 v211, v211
	v_fmamk_f32 v210, v210, 0xc0b8aa3b, v198
	v_fma_f32 v133, v201, v209, v205
	v_mfma_f32_32x32x2_f32 v[96:111], v248, v228, v[232:247]
	v_mfma_f32_32x32x16_f16 v[32:47], a[136:139], v[176:179], v[32:47]
	ds_read_b128 v[176:179], v193 offset:12288
	v_rcp_f32_e32 v212, v212
	v_fmamk_f32 v211, v211, 0xc0b8aa3b, v198
	v_fma_f32 v134, v202, v210, v206
	v_mfma_f32_32x32x2_f32 v[112:127], v248, v229, v[232:247]
	v_mfma_f32_32x32x16_f16 v[48:63], a[136:139], v[180:183], v[48:63]
	ds_read_b128 v[180:183], v193 offset:13312
	v_rcp_f32_e32 v213, v213
	v_fma_f32 v135, v203, v211, v207
	v_mfma_f32_32x32x16_f16 v[32:47], a[140:143], v[184:187], v[32:47]
	ds_read_b128 v[184:187], v193 offset:14336
	v_rcp_f32_e32 v214, v214
	v_mfma_f32_32x32x16_f16 v[48:63], a[140:143], v[188:191], v[48:63]
	ds_read_b128 v[188:191], v193 offset:15360
	global_load_lds_dwordx4 v192, s[44:45] offset:2048 sc1
	v_rcp_f32_e32 v215, v215
	s_waitcnt lgkmcnt(2)
	v_mfma_f32_32x32x16_f16 v[32:47], a[144:147], v[160:163], v[32:47]
	ds_read_b128 v[160:163], v193 offset:16384
	v_exp_f32_e32 v200, v132
	v_mfma_f32_32x32x16_f16 v[48:63], a[144:147], v[164:167], v[48:63]
	ds_read_b128 v[164:167], v193 offset:17408
	v_exp_f32_e32 v201, v133
	v_add_f32_e32 v200, 1.0, v200
	v_mfma_f32_32x32x16_f16 v[32:47], a[148:151], v[168:171], v[32:47]
	ds_read_b128 v[168:171], v193 offset:18432
	v_exp_f32_e32 v202, v134
	v_add_f32_e32 v201, 1.0, v201
	v_mfma_f32_32x32x16_f16 v[48:63], a[148:151], v[172:175], v[48:63]
	ds_read_b128 v[172:175], v193 offset:19456
	global_load_lds_dwordx4 v192, s[44:45] offset:3072 sc1
	v_exp_f32_e32 v203, v135
	v_add_f32_e32 v202, 1.0, v202
	v_mfma_f32_32x32x16_f16 v[32:47], a[152:155], v[176:179], v[32:47]
	ds_read_b128 v[176:179], v193 offset:20480
	v_add_f32_e32 v203, 1.0, v203
	v_rcp_f32_e32 v200, v200
	v_mfma_f32_32x32x16_f16 v[48:63], a[152:155], v[180:183], v[48:63]
	ds_read_b128 v[180:183], v193 offset:21504
	v_rcp_f32_e32 v201, v201
	v_fma_f32 v200, v200, 2.0, -1.0
	s_waitcnt lgkmcnt(2)
	v_mfma_f32_32x32x16_f16 v[32:47], a[156:159], v[184:187], v[32:47]
	ds_read_b128 v[184:187], v193 offset:22528
	v_rcp_f32_e32 v202, v202
	v_fma_f32 v201, v201, 2.0, -1.0
	v_mul_f32_e32 v216, v212, v200
	v_mfma_f32_32x32x16_f16 v[48:63], a[156:159], v[188:191], v[48:63]
	ds_read_b128 v[188:191], v193 offset:23552
	s_mov_b32 m0, s53
	s_add_u32 s44, s34, 0x1000
	s_addc_u32 s45, s35, 0
	global_load_lds_dwordx4 v192, s[44:45] sc1
	v_rcp_f32_e32 v203, v203
	v_fma_f32 v202, v202, 2.0, -1.0
	v_mul_f32_e32 v217, v213, v201
	v_mfma_f32_32x32x16_f16 v[32:47], a[160:163], v[160:163], v[32:47]
	ds_read_b128 v[160:163], v193 offset:24576
	v_fma_f32 v203, v203, 2.0, -1.0
	v_mul_f32_e32 v218, v214, v202
	v_mfma_f32_32x32x16_f16 v[48:63], a[160:163], v[164:167], v[48:63]
	ds_read_b128 v[164:167], v193 offset:25600
	v_mul_f32_e32 v219, v215, v203
	v_cvt_pk_f16_f32 v222, v216, v217
	v_mfma_f32_32x32x16_f16 v[32:47], a[164:167], v[168:171], v[32:47]
	ds_read_b128 v[168:171], v193 offset:26624
	v_cvt_pk_f16_f32 v223, v218, v219
	v_mfma_f32_32x32x16_f16 v[48:63], a[164:167], v[172:175], v[48:63]
	ds_read_b128 v[172:175], v193 offset:27648
	global_load_lds_dwordx4 v192, s[44:45] offset:1024 sc1
	s_cmp_eq_u32 s33, s60
	s_cbranch_scc1 .LE_ht26

.LE_htb33:
	v_exp_f32_e32 v203, v51
	v_mfma_f32_32x32x16_f16 v[64:79], a[88:91], v[176:179], v[64:79]
	ds_read_b128 v[176:179], v192 offset:53248
	v_exp_f32_e32 v204, v52
	v_add_f32_e32 v201, 1.0, v201
	v_add_f32_e32 v202, 1.0, v202
	v_mfma_f32_32x32x16_f16 v[80:95], a[88:91], v[180:183], v[80:95]
	ds_read_b128 v[180:183], v192 offset:54272
	v_exp_f32_e32 v205, v53
	v_add_f32_e32 v203, 1.0, v203
	v_add_f32_e32 v204, 1.0, v204
	v_mfma_f32_32x32x16_f16 v[64:79], a[92:95], v[184:187], v[64:79]
	ds_read_b128 v[184:187], v192 offset:55296
	v_exp_f32_e32 v206, v54
	v_add_f32_e32 v205, 1.0, v205
	v_mfma_f32_32x32x16_f16 v[80:95], a[92:95], v[188:191], v[80:95]
	ds_read_b128 v[188:191], v192 offset:56320
	s_mov_b32 m0, s59
	s_add_u32 s44, s34, 0x19000
	s_addc_u32 s45, s35, 0
	global_load_lds_dwordx4 v192, s[44:45] sc1
	v_exp_f32_e32 v207, v55
	v_add_f32_e32 v206, 1.0, v206
	s_waitcnt lgkmcnt(2)
	v_mfma_f32_32x32x16_f16 v[64:79], a[96:99], v[160:163], v[64:79]
	ds_read_b128 v[160:163], v192 offset:57344
	v_exp_f32_e32 v208, v56
	v_add_f32_e32 v207, 1.0, v207
	v_mfma_f32_32x32x16_f16 v[80:95], a[96:99], v[164:167], v[80:95]
	ds_read_b128 v[164:167], v192 offset:58368
	v_exp_f32_e32 v209, v57
	v_add_f32_e32 v208, 1.0, v208
	v_mfma_f32_32x32x16_f16 v[64:79], a[100:103], v[168:171], v[64:79]
	ds_read_b128 v[168:171], v192 offset:59392
	v_exp_f32_e32 v210, v58
	v_add_f32_e32 v209, 1.0, v209
	v_mfma_f32_32x32x16_f16 v[80:95], a[100:103], v[172:175], v[80:95]
	ds_read_b128 v[172:175], v192 offset:60416
	global_load_lds_dwordx4 v192, s[44:45] offset:1024 sc1
	v_exp_f32_e32 v211, v59
	v_add_f32_e32 v210, 1.0, v210
	v_mfma_f32_32x32x16_f16 v[64:79], a[104:107], v[176:179], v[64:79]
	ds_read_b128 v[176:179], v192 offset:61440
	v_exp_f32_e32 v212, v60
	v_add_f32_e32 v211, 1.0, v211
	v_mfma_f32_32x32x16_f16 v[80:95], a[104:107], v[180:183], v[80:95]
	ds_read_b128 v[180:183], v192 offset:62464
	v_exp_f32_e32 v213, v61
	v_add_f32_e32 v212, 1.0, v212
	s_waitcnt lgkmcnt(2)
	v_mfma_f32_32x32x16_f16 v[64:79], a[108:111], v[184:187], v[64:79]
	ds_read_b128 v[184:187], v192 offset:63488
	v_exp_f32_e32 v214, v62
	v_add_f32_e32 v213, 1.0, v213
	v_mfma_f32_32x32x16_f16 v[80:95], a[108:111], v[188:191], v[80:95]
	ds_read_b128 v[188:191], v192 offset:64512
	global_load_lds_dwordx4 v192, s[44:45] offset:2048 sc1
	v_exp_f32_e32 v215, v63
	v_add_f32_e32 v214, 1.0, v214
	s_waitcnt vmcnt(7)
	s_barrier
	v_mfma_f32_32x32x16_f16 v[64:79], a[112:115], v[160:163], v[64:79]
	ds_read_b128 v[160:163], v193 offset:0
	v_add_f32_e32 v215, 1.0, v215
	v_rcp_f32_e32 v200, v200
	v_mfma_f32_32x32x16_f16 v[80:95], a[112:115], v[164:167], v[80:95]
	ds_read_b128 v[164:167], v193 offset:1024
	v_rcp_f32_e32 v201, v201
	v_mfma_f32_32x32x16_f16 v[64:79], a[116:119], v[168:171], v[64:79]
	ds_read_b128 v[168:171], v193 offset:2048
	v_rcp_f32_e32 v202, v202
	v_mfma_f32_32x32x16_f16 v[80:95], a[116:119], v[172:175], v[80:95]
	ds_read_b128 v[172:175], v193 offset:3072
	global_load_lds_dwordx4 v192, s[44:45] offset:3072 sc1
	v_rcp_f32_e32 v203, v203
	s_waitcnt lgkmcnt(2)
	v_mfma_f32_32x32x16_f16 v[64:79], a[120:123], v[176:179], v[64:79]
	ds_read_b128 v[176:179], v193 offset:4096
	v_rcp_f32_e32 v204, v204
	v_mfma_f32_32x32x16_f16 v[80:95], a[120:123], v[180:183], v[80:95]
	ds_read_b128 v[180:183], v193 offset:5120
	v_rcp_f32_e32 v205, v205
	v_mul_f32_e32 v204, v204, v140
	v_mfma_f32_32x32x16_f16 v[64:79], a[124:127], v[184:187], v[64:79]
	ds_read_b128 v[184:187], v193 offset:6144
	v_rcp_f32_e32 v206, v206
	v_mul_f32_e32 v205, v205, v141
	v_mfma_f32_32x32x16_f16 v[80:95], a[124:127], v[188:191], v[80:95]
	ds_read_b128 v[188:191], v193 offset:7168
	v_cmp_gt_u32_e32 vcc, 4, v251
	s_cbranch_vccnz .LE_tpoll35
.LE_tok34:
	s_and_b32 s64, s71, 1
	s_lshl_b32 s64, s64, 22
	s_add_u32 s64, s64, s49
	s_add_u32 s64, s64, 0x60000
	s_add_u32 s34, s6, s64
	s_addc_u32 s35, s7, 0
	s_mov_b32 m0, s52
	s_add_u32 s44, s34, 0x0
	s_addc_u32 s45, s35, 0
	global_load_lds_dwordx4 v192, s[44:45] sc1
	v_rcp_f32_e32 v207, v207
	v_mul_f32_e32 v206, v206, v142
	v_mfma_f32_32x32x16_f16 v[64:79], a[128:131], v[160:163], v[64:79]
	ds_read_b128 v[160:163], v193 offset:8192
	v_rcp_f32_e32 v208, v208
	v_mul_f32_e32 v207, v207, v143
	v_mfma_f32_32x32x16_f16 v[80:95], a[128:131], v[164:167], v[80:95]
	ds_read_b128 v[164:167], v193 offset:9216
	v_rcp_f32_e32 v209, v209
	v_fmamk_f32 v208, v208, 0xc0b8aa3b, v198
	s_waitcnt lgkmcnt(2)
	v_mfma_f32_32x32x16_f16 v[64:79], a[132:135], v[168:171], v[64:79]
	ds_read_b128 v[168:171], v193 offset:10240
	v_rcp_f32_e32 v210, v210
	v_fmamk_f32 v209, v209, 0xc0b8aa3b, v198
	v_fma_f32 v140, v200, v208, v204
	v_mfma_f32_32x32x16_f16 v[80:95], a[132:135], v[172:175], v[80:95]
	ds_read_b128 v[172:175], v193 offset:11264
	global_load_lds_dwordx4 v192, s[44:45] offset:1024 sc1
	v_rcp_f32_e32 v211, v211
	v_fmamk_f32 v210, v210, 0xc0b8aa3b, v198
	v_fma_f32 v141, v201, v209, v205
	v_mfma_f32_32x32x2_f32 v[0:15], v248, v228, v[232:247]
	v_mfma_f32_32x32x16_f16 v[64:79], a[136:139], v[176:179], v[64:79]
	ds_read_b128 v[176:179], v193 offset:12288
	v_rcp_f32_e32 v212, v212
	v_fmamk_f32 v211, v211, 0xc0b8aa3b, v198
	v_fma_f32 v142, v202, v210, v206
	v_mfma_f32_32x32x2_f32 v[16:31], v248, v229, v[232:247]
	v_mfma_f32_32x32x16_f16 v[80:95], a[136:139], v[180:183], v[80:95]
	ds_read_b128 v[180:183], v193 offset:13312
	v_rcp_f32_e32 v213, v213
	v_fma_f32 v143, v203, v211, v207
	v_mfma_f32_32x32x16_f16 v[64:79], a[140:143], v[184:187], v[64:79]
	ds_read_b128 v[184:187], v193 offset:14336
	v_rcp_f32_e32 v214, v214
	v_mfma_f32_32x32x16_f16 v[80:95], a[140:143], v[188:191], v[80:95]
	ds_read_b128 v[188:191], v193 offset:15360
	global_load_lds_dwordx4 v192, s[44:45] offset:2048 sc1
	v_rcp_f32_e32 v215, v215
	s_waitcnt lgkmcnt(2)
	v_mfma_f32_32x32x16_f16 v[64:79], a[144:147], v[160:163], v[64:79]
	ds_read_b128 v[160:163], v193 offset:16384
	v_exp_f32_e32 v200, v140
	v_mfma_f32_32x32x16_f16 v[80:95], a[144:147], v[164:167], v[80:95]
	ds_read_b128 v[164:167], v193 offset:17408
	v_exp_f32_e32 v201, v141
	v_add_f32_e32 v200, 1.0, v200
	v_mfma_f32_32x32x16_f16 v[64:79], a[148:151], v[168:171], v[64:79]
	ds_read_b128 v[168:171], v193 offset:18432
	v_exp_f32_e32 v202, v142
	v_add_f32_e32 v201, 1.0, v201
	v_mfma_f32_32x32x16_f16 v[80:95], a[148:151], v[172:175], v[80:95]
	ds_read_b128 v[172:175], v193 offset:19456
	global_load_lds_dwordx4 v192, s[44:45] offset:3072 sc1
	v_exp_f32_e32 v203, v143
	v_add_f32_e32 v202, 1.0, v202
	v_mfma_f32_32x32x16_f16 v[64:79], a[152:155], v[176:179], v[64:79]
	ds_read_b128 v[176:179], v193 offset:20480
	v_add_f32_e32 v203, 1.0, v203
	v_rcp_f32_e32 v200, v200
	v_mfma_f32_32x32x16_f16 v[80:95], a[152:155], v[180:183], v[80:95]
	ds_read_b128 v[180:183], v193 offset:21504
	v_rcp_f32_e32 v201, v201
	v_fma_f32 v200, v200, 2.0, -1.0
	s_waitcnt lgkmcnt(2)
	v_mfma_f32_32x32x16_f16 v[64:79], a[156:159], v[184:187], v[64:79]
	ds_read_b128 v[184:187], v193 offset:22528
	v_rcp_f32_e32 v202, v202
	v_fma_f32 v201, v201, 2.0, -1.0
	v_mul_f32_e32 v216, v212, v200
	v_mfma_f32_32x32x16_f16 v[80:95], a[156:159], v[188:191], v[80:95]
	ds_read_b128 v[188:191], v193 offset:23552
	s_mov_b32 m0, s53
	s_add_u32 s44, s34, 0x1000
	s_addc_u32 s45, s35, 0
	global_load_lds_dwordx4 v192, s[44:45] sc1
	v_rcp_f32_e32 v203, v203
	v_fma_f32 v202, v202, 2.0, -1.0
	v_mul_f32_e32 v217, v213, v201
	v_mfma_f32_32x32x16_f16 v[64:79], a[160:163], v[160:163], v[64:79]
	ds_read_b128 v[160:163], v193 offset:24576
	v_fma_f32 v203, v203, 2.0, -1.0
	v_mul_f32_e32 v218, v214, v202
	v_mfma_f32_32x32x16_f16 v[80:95], a[160:163], v[164:167], v[80:95]
	ds_read_b128 v[164:167], v193 offset:25600
	v_mul_f32_e32 v219, v215, v203
	v_cvt_pk_f16_f32 v222, v216, v217
	v_mfma_f32_32x32x16_f16 v[64:79], a[164:167], v[168:171], v[64:79]
	ds_read_b128 v[168:171], v193 offset:26624
	v_cvt_pk_f16_f32 v223, v218, v219
	v_mfma_f32_32x32x16_f16 v[80:95], a[164:167], v[172:175], v[80:95]
	ds_read_b128 v[172:175], v193 offset:27648
	global_load_lds_dwordx4 v192, s[44:45] offset:1024 sc1
	s_cmp_eq_u32 s33, s60
	s_cbranch_scc1 .LE_ht36

.LE_htb43:
	v_exp_f32_e32 v203, v83
	v_mfma_f32_32x32x16_f16 v[96:111], a[88:91], v[176:179], v[96:111]
	ds_read_b128 v[176:179], v192 offset:53248
	v_exp_f32_e32 v204, v84
	v_add_f32_e32 v201, 1.0, v201
	v_add_f32_e32 v202, 1.0, v202
	v_mfma_f32_32x32x16_f16 v[112:127], a[88:91], v[180:183], v[112:127]
	ds_read_b128 v[180:183], v192 offset:54272
	v_exp_f32_e32 v205, v85
	v_add_f32_e32 v203, 1.0, v203
	v_add_f32_e32 v204, 1.0, v204
	v_mfma_f32_32x32x16_f16 v[96:111], a[92:95], v[184:187], v[96:111]
	ds_read_b128 v[184:187], v192 offset:55296
	v_exp_f32_e32 v206, v86
	v_add_f32_e32 v205, 1.0, v205
	v_mfma_f32_32x32x16_f16 v[112:127], a[92:95], v[188:191], v[112:127]
	ds_read_b128 v[188:191], v192 offset:56320
	s_mov_b32 m0, s59
	s_add_u32 s44, s34, 0x19000
	s_addc_u32 s45, s35, 0
	global_load_lds_dwordx4 v192, s[44:45] sc1
	v_exp_f32_e32 v207, v87
	v_add_f32_e32 v206, 1.0, v206
	s_waitcnt lgkmcnt(2)
	v_mfma_f32_32x32x16_f16 v[96:111], a[96:99], v[160:163], v[96:111]
	ds_read_b128 v[160:163], v192 offset:57344
	v_exp_f32_e32 v208, v88
	v_add_f32_e32 v207, 1.0, v207
	v_mfma_f32_32x32x16_f16 v[112:127], a[96:99], v[164:167], v[112:127]
	ds_read_b128 v[164:167], v192 offset:58368
	v_exp_f32_e32 v209, v89
	v_add_f32_e32 v208, 1.0, v208
	v_mfma_f32_32x32x16_f16 v[96:111], a[100:103], v[168:171], v[96:111]
	ds_read_b128 v[168:171], v192 offset:59392
	v_exp_f32_e32 v210, v90
	v_add_f32_e32 v209, 1.0, v209
	v_mfma_f32_32x32x16_f16 v[112:127], a[100:103], v[172:175], v[112:127]
	ds_read_b128 v[172:175], v192 offset:60416
	global_load_lds_dwordx4 v192, s[44:45] offset:1024 sc1
	v_exp_f32_e32 v211, v91
	v_add_f32_e32 v210, 1.0, v210
	v_mfma_f32_32x32x16_f16 v[96:111], a[104:107], v[176:179], v[96:111]
	ds_read_b128 v[176:179], v192 offset:61440
	v_exp_f32_e32 v212, v92
	v_add_f32_e32 v211, 1.0, v211
	v_mfma_f32_32x32x16_f16 v[112:127], a[104:107], v[180:183], v[112:127]
	ds_read_b128 v[180:183], v192 offset:62464
	v_exp_f32_e32 v213, v93
	v_add_f32_e32 v212, 1.0, v212
	s_waitcnt lgkmcnt(2)
	v_mfma_f32_32x32x16_f16 v[96:111], a[108:111], v[184:187], v[96:111]
	ds_read_b128 v[184:187], v192 offset:63488
	v_exp_f32_e32 v214, v94
	v_add_f32_e32 v213, 1.0, v213
	v_mfma_f32_32x32x16_f16 v[112:127], a[108:111], v[188:191], v[112:127]
	ds_read_b128 v[188:191], v192 offset:64512
	global_load_lds_dwordx4 v192, s[44:45] offset:2048 sc1
	v_exp_f32_e32 v215, v95
	v_add_f32_e32 v214, 1.0, v214
	s_waitcnt vmcnt(7)
	s_barrier
	v_mfma_f32_32x32x16_f16 v[96:111], a[112:115], v[160:163], v[96:111]
	ds_read_b128 v[160:163], v193 offset:0
	v_add_f32_e32 v215, 1.0, v215
	v_rcp_f32_e32 v200, v200
	v_mfma_f32_32x32x16_f16 v[112:127], a[112:115], v[164:167], v[112:127]
	ds_read_b128 v[164:167], v193 offset:1024
	v_rcp_f32_e32 v201, v201
	v_mfma_f32_32x32x16_f16 v[96:111], a[116:119], v[168:171], v[96:111]
	ds_read_b128 v[168:171], v193 offset:2048
	v_rcp_f32_e32 v202, v202
	v_mfma_f32_32x32x16_f16 v[112:127], a[116:119], v[172:175], v[112:127]
	ds_read_b128 v[172:175], v193 offset:3072
	global_load_lds_dwordx4 v192, s[44:45] offset:3072 sc1
	v_rcp_f32_e32 v203, v203
	s_waitcnt lgkmcnt(2)
	v_mfma_f32_32x32x16_f16 v[96:111], a[120:123], v[176:179], v[96:111]
	ds_read_b128 v[176:179], v193 offset:4096
	v_rcp_f32_e32 v204, v204
	v_mfma_f32_32x32x16_f16 v[112:127], a[120:123], v[180:183], v[112:127]
	ds_read_b128 v[180:183], v193 offset:5120
	v_rcp_f32_e32 v205, v205
	v_mul_f32_e32 v204, v204, v148
	v_mfma_f32_32x32x16_f16 v[96:111], a[124:127], v[184:187], v[96:111]
	ds_read_b128 v[184:187], v193 offset:6144
	v_rcp_f32_e32 v206, v206
	v_mul_f32_e32 v205, v205, v149
	v_mfma_f32_32x32x16_f16 v[112:127], a[124:127], v[188:191], v[112:127]
	ds_read_b128 v[188:191], v193 offset:7168
	v_cmp_gt_u32_e32 vcc, 1, v251
	s_cbranch_vccnz .LE_tpoll45
.LE_tok44:
	s_and_b32 s64, s33, 1
	s_lshl_b32 s64, s64, 22
	s_add_u32 s64, s64, s49
	s_add_u32 s34, s6, s64
	s_addc_u32 s35, s7, 0
	s_mov_b32 m0, s52
	s_add_u32 s44, s34, 0x0
	s_addc_u32 s45, s35, 0
	global_load_lds_dwordx4 v192, s[44:45] sc1
	v_rcp_f32_e32 v207, v207
	v_mul_f32_e32 v206, v206, v150
	v_mfma_f32_32x32x16_f16 v[96:111], a[128:131], v[160:163], v[96:111]
	ds_read_b128 v[160:163], v193 offset:8192
	v_rcp_f32_e32 v208, v208
	v_mul_f32_e32 v207, v207, v151
	v_mfma_f32_32x32x16_f16 v[112:127], a[128:131], v[164:167], v[112:127]
	ds_read_b128 v[164:167], v193 offset:9216
	v_rcp_f32_e32 v209, v209
	v_fmamk_f32 v208, v208, 0xc0b8aa3b, v198
	s_waitcnt lgkmcnt(2)
	v_mfma_f32_32x32x16_f16 v[96:111], a[132:135], v[168:171], v[96:111]
	ds_read_b128 v[168:171], v193 offset:10240
	v_rcp_f32_e32 v210, v210
	v_fmamk_f32 v209, v209, 0xc0b8aa3b, v198
	v_fma_f32 v148, v200, v208, v204
	v_mfma_f32_32x32x16_f16 v[112:127], a[132:135], v[172:175], v[112:127]
	ds_read_b128 v[172:175], v193 offset:11264
	global_load_lds_dwordx4 v192, s[44:45] offset:1024 sc1
	v_rcp_f32_e32 v211, v211
	v_fmamk_f32 v210, v210, 0xc0b8aa3b, v198
	v_fma_f32 v149, v201, v209, v205
	v_mfma_f32_32x32x2_f32 v[32:47], v248, v228, v[232:247]
	v_mfma_f32_32x32x16_f16 v[96:111], a[136:139], v[176:179], v[96:111]
	ds_read_b128 v[176:179], v193 offset:12288
	v_rcp_f32_e32 v212, v212
	v_fmamk_f32 v211, v211, 0xc0b8aa3b, v198
	v_fma_f32 v150, v202, v210, v206
	v_mfma_f32_32x32x2_f32 v[48:63], v248, v229, v[232:247]
	v_mfma_f32_32x32x16_f16 v[112:127], a[136:139], v[180:183], v[112:127]
	ds_read_b128 v[180:183], v193 offset:13312
	v_rcp_f32_e32 v213, v213
	v_fma_f32 v151, v203, v211, v207
	v_mfma_f32_32x32x16_f16 v[96:111], a[140:143], v[184:187], v[96:111]
	ds_read_b128 v[184:187], v193 offset:14336
	v_rcp_f32_e32 v214, v214
	v_mfma_f32_32x32x16_f16 v[112:127], a[140:143], v[188:191], v[112:127]
	ds_read_b128 v[188:191], v193 offset:15360
	global_load_lds_dwordx4 v192, s[44:45] offset:2048 sc1
	v_rcp_f32_e32 v215, v215
	s_waitcnt lgkmcnt(2)
	v_mfma_f32_32x32x16_f16 v[96:111], a[144:147], v[160:163], v[96:111]
	ds_read_b128 v[160:163], v193 offset:16384
	v_exp_f32_e32 v200, v148
	v_mfma_f32_32x32x16_f16 v[112:127], a[144:147], v[164:167], v[112:127]
	ds_read_b128 v[164:167], v193 offset:17408
	v_exp_f32_e32 v201, v149
	v_add_f32_e32 v200, 1.0, v200
	v_mfma_f32_32x32x16_f16 v[96:111], a[148:151], v[168:171], v[96:111]
	ds_read_b128 v[168:171], v193 offset:18432
	v_exp_f32_e32 v202, v150
	v_add_f32_e32 v201, 1.0, v201
	v_mfma_f32_32x32x16_f16 v[112:127], a[148:151], v[172:175], v[112:127]
	ds_read_b128 v[172:175], v193 offset:19456
	global_load_lds_dwordx4 v192, s[44:45] offset:3072 sc1
	v_exp_f32_e32 v203, v151
	v_add_f32_e32 v202, 1.0, v202
	v_mfma_f32_32x32x16_f16 v[96:111], a[152:155], v[176:179], v[96:111]
	ds_read_b128 v[176:179], v193 offset:20480
	v_add_f32_e32 v203, 1.0, v203
	v_rcp_f32_e32 v200, v200
	v_mfma_f32_32x32x16_f16 v[112:127], a[152:155], v[180:183], v[112:127]
	ds_read_b128 v[180:183], v193 offset:21504
	v_rcp_f32_e32 v201, v201
	v_fma_f32 v200, v200, 2.0, -1.0
	s_waitcnt lgkmcnt(2)
	v_mfma_f32_32x32x16_f16 v[96:111], a[156:159], v[184:187], v[96:111]
	ds_read_b128 v[184:187], v193 offset:22528
	v_rcp_f32_e32 v202, v202
	v_fma_f32 v201, v201, 2.0, -1.0
	v_mul_f32_e32 v216, v212, v200
	v_mfma_f32_32x32x16_f16 v[112:127], a[156:159], v[188:191], v[112:127]
	ds_read_b128 v[188:191], v193 offset:23552
	s_mov_b32 m0, s53
	s_add_u32 s44, s34, 0x1000
	s_addc_u32 s45, s35, 0
	global_load_lds_dwordx4 v192, s[44:45] sc1
	v_rcp_f32_e32 v203, v203
	v_fma_f32 v202, v202, 2.0, -1.0
	v_mul_f32_e32 v217, v213, v201
	v_mfma_f32_32x32x16_f16 v[96:111], a[160:163], v[160:163], v[96:111]
	ds_read_b128 v[160:163], v193 offset:24576
	v_fma_f32 v203, v203, 2.0, -1.0
	v_mul_f32_e32 v218, v214, v202
	v_mfma_f32_32x32x16_f16 v[112:127], a[160:163], v[164:167], v[112:127]
	ds_read_b128 v[164:167], v193 offset:25600
	v_mul_f32_e32 v219, v215, v203
	v_cvt_pk_f16_f32 v222, v216, v217
	v_mfma_f32_32x32x16_f16 v[96:111], a[164:167], v[168:171], v[96:111]
	ds_read_b128 v[168:171], v193 offset:26624
	v_cvt_pk_f16_f32 v223, v218, v219
	v_mfma_f32_32x32x16_f16 v[112:127], a[164:167], v[172:175], v[112:127]
	ds_read_b128 v[172:175], v193 offset:27648
	global_load_lds_dwordx4 v192, s[44:45] offset:1024 sc1
	s_cmp_eq_u32 s33, s60
	s_cbranch_scc1 .LE_ht46

.LD_loop12:
	s_sub_u32 s71, s33, 1
	s_add_u32 s61, s33, 1
	s_min_u32 s61, s61, s60
	s_and_b32 s64, s71, 1
	s_lshl_b32 s64, s64, 22
	s_add_u32 s64, s64, s50
	s_add_u32 s64, s64, 0x60000
	s_add_u32 s36, s6, s64
	s_addc_u32 s37, s7, 0
	s_lshl_b32 s64, s71, 3
	s_add_u32 s64, s64, s29
	s_lshl_b32 s64, s64, 5
	s_add_u32 s64, s64, s30
	s_lshl_b32 s64, s64, 2
	s_add_u32 s40, s8, s64
	s_addc_u32 s41, s9, 0
	s_lshl_b32 s64, s71, 19
	s_add_u32 s64, s64, 0x600
	s_add_u32 s72, s62, s64
	s_addc_u32 s73, s63, 0
	s_nop 3
	s_waitcnt lgkmcnt(2)
	v_mfma_f32_32x32x16_f16 v[0:15], a[0:3], v[160:163], v[0:15]
	ds_read_b128 v[160:163], v192 offset:8192
	v_exp_f32_e32 v200, v96
	v_mfma_f32_32x32x16_f16 v[16:31], a[0:3], v[164:167], v[16:31]
	ds_read_b128 v[164:167], v192 offset:9216
	s_lshl_b32 s64, s71, 3
	s_add_u32 s64, s64, s29
	s_lshl_b32 s64, s64, 7
	s_add_u32 s38, s8, s64
	s_addc_u32 s39, s9, 0
	global_load_dword v251, v196, s[38:39] sc1
	v_exp_f32_e32 v201, v97
	v_add_f32_e32 v200, 1.0, v200
	v_mfma_f32_32x32x16_f16 v[0:15], a[4:7], v[168:171], v[0:15]
	ds_read_b128 v[168:171], v192 offset:10240
	v_exp_f32_e32 v202, v98
	v_add_f32_e32 v201, 1.0, v201
	v_mfma_f32_32x32x16_f16 v[16:31], a[4:7], v[172:175], v[16:31]
	ds_read_b128 v[172:175], v192 offset:11264
	global_load_lds_dwordx4 v192, s[44:45] offset:1024 sc1
	v_exp_f32_e32 v203, v99
	v_add_f32_e32 v202, 1.0, v202
	v_mfma_f32_32x32x16_f16 v[0:15], a[8:11], v[176:179], v[0:15]
	ds_read_b128 v[176:179], v192 offset:12288
	v_exp_f32_e32 v204, v100
	v_add_f32_e32 v203, 1.0, v203
	v_mfma_f32_32x32x16_f16 v[16:31], a[8:11], v[180:183], v[16:31]
	ds_read_b128 v[180:183], v192 offset:13312
	v_exp_f32_e32 v205, v101
	v_add_f32_e32 v204, 1.0, v204
	s_waitcnt lgkmcnt(2)
	v_mfma_f32_32x32x16_f16 v[0:15], a[12:15], v[184:187], v[0:15]
	ds_read_b128 v[184:187], v192 offset:14336
	v_exp_f32_e32 v206, v102
	v_add_f32_e32 v205, 1.0, v205
	v_mfma_f32_32x32x16_f16 v[16:31], a[12:15], v[188:191], v[16:31]
	ds_read_b128 v[188:191], v192 offset:15360
	global_load_lds_dwordx4 v192, s[44:45] offset:2048 sc1
	v_exp_f32_e32 v207, v103
	v_add_f32_e32 v206, 1.0, v206
	v_mfma_f32_32x32x16_f16 v[0:15], a[16:19], v[160:163], v[0:15]
	ds_read_b128 v[160:163], v192 offset:16384
	v_exp_f32_e32 v208, v104
	v_add_f32_e32 v207, 1.0, v207
	v_mfma_f32_32x32x16_f16 v[16:31], a[16:19], v[164:167], v[16:31]
	ds_read_b128 v[164:167], v192 offset:17408
	v_exp_f32_e32 v209, v105
	v_add_f32_e32 v208, 1.0, v208
	v_mfma_f32_32x32x16_f16 v[0:15], a[20:23], v[168:171], v[0:15]
	ds_read_b128 v[168:171], v192 offset:18432
	v_exp_f32_e32 v210, v106
	v_add_f32_e32 v209, 1.0, v209
	v_mfma_f32_32x32x16_f16 v[16:31], a[20:23], v[172:175], v[16:31]
	ds_read_b128 v[172:175], v192 offset:19456
	global_load_lds_dwordx4 v192, s[44:45] offset:3072 sc1
	v_exp_f32_e32 v211, v107
	v_add_f32_e32 v210, 1.0, v210
	s_waitcnt lgkmcnt(2)
	v_mfma_f32_32x32x16_f16 v[0:15], a[24:27], v[176:179], v[0:15]
	ds_read_b128 v[176:179], v192 offset:20480
	v_exp_f32_e32 v212, v108
	v_add_f32_e32 v211, 1.0, v211
	v_mfma_f32_32x32x16_f16 v[16:31], a[24:27], v[180:183], v[16:31]
	ds_read_b128 v[180:183], v192 offset:21504
	v_exp_f32_e32 v213, v109
	v_add_f32_e32 v212, 1.0, v212
	v_mfma_f32_32x32x16_f16 v[0:15], a[28:31], v[184:187], v[0:15]
	ds_read_b128 v[184:187], v192 offset:22528
	v_exp_f32_e32 v214, v110
	v_add_f32_e32 v213, 1.0, v213
	v_mfma_f32_32x32x16_f16 v[16:31], a[28:31], v[188:191], v[16:31]
	ds_read_b128 v[188:191], v192 offset:23552
	s_mov_b32 m0, s57
	s_add_u32 s44, s34, 0x11000
	s_addc_u32 s45, s35, 0
	global_load_lds_dwordx4 v192, s[44:45] sc1
	v_exp_f32_e32 v215, v111
	v_add_f32_e32 v214, 1.0, v214
	v_mfma_f32_32x32x16_f16 v[0:15], a[32:35], v[160:163], v[0:15]
	ds_read_b128 v[160:163], v192 offset:24576
	v_add_f32_e32 v215, 1.0, v215
	v_rcp_f32_e32 v200, v200
	v_mfma_f32_32x32x16_f16 v[16:31], a[32:35], v[164:167], v[16:31]
	ds_read_b128 v[164:167], v192 offset:25600
	v_rcp_f32_e32 v201, v201
	s_waitcnt lgkmcnt(2)
	v_mfma_f32_32x32x16_f16 v[0:15], a[36:39], v[168:171], v[0:15]
	ds_read_b128 v[168:171], v192 offset:26624
	v_rcp_f32_e32 v202, v202
	v_mfma_f32_32x32x16_f16 v[16:31], a[36:39], v[172:175], v[16:31]
	ds_read_b128 v[172:175], v192 offset:27648
	global_load_lds_dwordx4 v192, s[44:45] offset:1024 sc1
	v_rcp_f32_e32 v203, v203
	v_mfma_f32_32x32x16_f16 v[0:15], a[40:43], v[176:179], v[0:15]
	ds_read_b128 v[176:179], v192 offset:28672
	v_rcp_f32_e32 v204, v204
	v_mfma_f32_32x32x16_f16 v[16:31], a[40:43], v[180:183], v[16:31]
	ds_read_b128 v[180:183], v192 offset:29696
	v_rcp_f32_e32 v205, v205
	v_mul_f32_e32 v204, v204, v152
	v_mfma_f32_32x32x16_f16 v[0:15], a[44:47], v[184:187], v[0:15]
	ds_read_b128 v[184:187], v192 offset:30720
	v_rcp_f32_e32 v206, v206
	v_mul_f32_e32 v205, v205, v153
	v_mfma_f32_32x32x16_f16 v[16:31], a[44:47], v[188:191], v[16:31]
	ds_read_b128 v[188:191], v192 offset:31744
	global_load_lds_dwordx4 v192, s[44:45] offset:2048 sc1
	v_rcp_f32_e32 v207, v207
	v_mul_f32_e32 v206, v206, v154
	s_waitcnt vmcnt(8)
	s_barrier
	s_waitcnt lgkmcnt(2)
	v_mfma_f32_32x32x16_f16 v[0:15], a[48:51], v[160:163], v[0:15]
	ds_read_b128 v[160:163], v192 offset:32768
	v_rcp_f32_e32 v208, v208
	v_mul_f32_e32 v207, v207, v155
	v_mfma_f32_32x32x16_f16 v[16:31], a[48:51], v[164:167], v[16:31]
	ds_read_b128 v[164:167], v192 offset:33792
	v_rcp_f32_e32 v209, v209
	v_fmamk_f32 v208, v208, 0xc0b8aa3b, v198
	v_mfma_f32_32x32x16_f16 v[0:15], a[52:55], v[168:171], v[0:15]
	ds_read_b128 v[168:171], v192 offset:34816
	v_rcp_f32_e32 v210, v210
	v_fmamk_f32 v209, v209, 0xc0b8aa3b, v198
	v_fma_f32 v152, v200, v208, v204
	v_mfma_f32_32x32x16_f16 v[16:31], a[52:55], v[172:175], v[16:31]
	ds_read_b128 v[172:175], v192 offset:35840
	global_load_lds_dwordx4 v192, s[44:45] offset:3072 sc1
	v_rcp_f32_e32 v211, v211
	v_fmamk_f32 v210, v210, 0xc0b8aa3b, v198
	v_fma_f32 v153, v201, v209, v205
	v_mfma_f32_32x32x16_f16 v[0:15], a[56:59], v[176:179], v[0:15]
	ds_read_b128 v[176:179], v192 offset:36864
	v_rcp_f32_e32 v212, v212
	v_fmamk_f32 v211, v211, 0xc0b8aa3b, v198
	v_fma_f32 v154, v202, v210, v206
	v_mfma_f32_32x32x16_f16 v[16:31], a[56:59], v[180:183], v[16:31]
	ds_read_b128 v[180:183], v192 offset:37888
	v_rcp_f32_e32 v213, v213
	v_fma_f32 v155, v203, v211, v207
	s_waitcnt lgkmcnt(2)
	v_mfma_f32_32x32x16_f16 v[0:15], a[60:63], v[184:187], v[0:15]
	ds_read_b128 v[184:187], v192 offset:38912
	v_rcp_f32_e32 v214, v214
	v_mfma_f32_32x32x16_f16 v[16:31], a[60:63], v[188:191], v[16:31]
	ds_read_b128 v[188:191], v192 offset:39936
	s_mov_b32 m0, s58
	s_add_u32 s44, s34, 0x18000
	s_addc_u32 s45, s35, 0
	global_load_lds_dwordx4 v192, s[44:45] sc1
	v_rcp_f32_e32 v215, v215
	v_mfma_f32_32x32x16_f16 v[0:15], a[64:67], v[160:163], v[0:15]
	ds_read_b128 v[160:163], v192 offset:40960
	v_exp_f32_e32 v200, v152
	v_mfma_f32_32x32x16_f16 v[16:31], a[64:67], v[164:167], v[16:31]
	ds_read_b128 v[164:167], v192 offset:41984
	v_exp_f32_e32 v201, v153
	v_add_f32_e32 v200, 1.0, v200
	v_mfma_f32_32x32x16_f16 v[0:15], a[68:71], v[168:171], v[0:15]
	ds_read_b128 v[168:171], v192 offset:43008
	v_exp_f32_e32 v202, v154
	v_add_f32_e32 v201, 1.0, v201
	v_mfma_f32_32x32x16_f16 v[16:31], a[68:71], v[172:175], v[16:31]
	ds_read_b128 v[172:175], v192 offset:44032
	global_load_lds_dwordx4 v192, s[44:45] offset:1024 sc1
	v_exp_f32_e32 v203, v155
	v_add_f32_e32 v202, 1.0, v202
	s_waitcnt lgkmcnt(2)
	v_mfma_f32_32x32x16_f16 v[0:15], a[72:75], v[176:179], v[0:15]
	ds_read_b128 v[176:179], v192 offset:45056
	v_add_f32_e32 v203, 1.0, v203
	v_rcp_f32_e32 v200, v200
	v_mfma_f32_32x32x16_f16 v[16:31], a[72:75], v[180:183], v[16:31]
	ds_read_b128 v[180:183], v192 offset:46080
	v_rcp_f32_e32 v201, v201
	v_fma_f32 v200, v200, 2.0, -1.0
	v_mfma_f32_32x32x16_f16 v[0:15], a[76:79], v[184:187], v[0:15]
	ds_read_b128 v[184:187], v192 offset:47104
	v_rcp_f32_e32 v202, v202
	v_fma_f32 v201, v201, 2.0, -1.0
	v_mul_f32_e32 v216, v212, v200
	v_mfma_f32_32x32x16_f16 v[16:31], a[76:79], v[188:191], v[16:31]
	ds_read_b128 v[188:191], v192 offset:48128
	global_load_lds_dwordx4 v192, s[44:45] offset:2048 sc1
	v_rcp_f32_e32 v203, v203
	v_fma_f32 v202, v202, 2.0, -1.0
	v_mul_f32_e32 v217, v213, v201
	v_mfma_f32_32x32x16_f16 v[0:15], a[80:83], v[160:163], v[0:15]
	ds_read_b128 v[160:163], v192 offset:49152
	v_fma_f32 v203, v203, 2.0, -1.0
	v_mul_f32_e32 v218, v214, v202
	v_exp_f32_e32 v200, v112
	v_mfma_f32_32x32x16_f16 v[16:31], a[80:83], v[164:167], v[16:31]
	ds_read_b128 v[164:167], v192 offset:50176
	v_mul_f32_e32 v219, v215, v203
	v_mul_f32_e32 v236, v216, v228
	v_exp_f32_e32 v201, v113
	s_waitcnt lgkmcnt(2)
	v_mfma_f32_32x32x16_f16 v[0:15], a[84:87], v[168:171], v[0:15]
	ds_read_b128 v[168:171], v192 offset:51200
	v_mul_f32_e32 v237, v216, v232
	v_fmac_f32_e32 v236, v217, v229
	v_exp_f32_e32 v202, v114
	v_mfma_f32_32x32x16_f16 v[16:31], a[84:87], v[172:175], v[16:31]
	ds_read_b128 v[172:175], v192 offset:52224
	global_load_lds_dwordx4 v192, s[44:45] offset:3072 sc1
	v_fmac_f32_e32 v237, v217, v233
	v_fmac_f32_e32 v236, v218, v230
	v_exp_f32_e32 v203, v115
	v_mfma_f32_32x32x16_f16 v[0:15], a[88:91], v[176:179], v[0:15]
	ds_read_b128 v[176:179], v192 offset:53248
	v_fmac_f32_e32 v237, v218, v234
	v_fmac_f32_e32 v236, v219, v231
	v_exp_f32_e32 v204, v116
	v_mfma_f32_32x32x16_f16 v[16:31], a[88:91], v[180:183], v[16:31]
	ds_read_b128 v[180:183], v192 offset:54272
	v_fmac_f32_e32 v237, v219, v235
	v_mov_b32_e32 v238, v236
	v_exp_f32_e32 v205, v117
	v_mfma_f32_32x32x16_f16 v[0:15], a[92:95], v[184:187], v[0:15]
	ds_read_b128 v[184:187], v192 offset:55296
	v_mov_b32_e32 v240, v237
	v_cvt_pk_f16_f32 v220, v216, v217
	v_exp_f32_e32 v206, v118
	v_mfma_f32_32x32x16_f16 v[16:31], a[92:95], v[188:191], v[16:31]
	ds_read_b128 v[188:191], v192 offset:56320
	s_mov_b32 m0, s59
	s_add_u32 s44, s34, 0x19000
	s_addc_u32 s45, s35, 0
	global_load_lds_dwordx4 v192, s[44:45] sc1
	v_permlane32_swap_b32_e32 v236, v238
	v_permlane32_swap_b32_e32 v237, v240
	v_add_f32_e32 v238, v236, v238
	v_add_f32_e32 v239, v237, v240
	ds_write_b64 v248, v[238:239] offset:1536
	v_exp_f32_e32 v207, v119
	s_waitcnt lgkmcnt(3)
	v_mfma_f32_32x32x16_f16 v[0:15], a[96:99], v[160:163], v[0:15]
	ds_read_b128 v[160:163], v192 offset:57344
	v_cvt_pk_f16_f32 v221, v218, v219
	v_exp_f32_e32 v208, v120
	v_add_f32_e32 v200, 1.0, v200
	v_mfma_f32_32x32x16_f16 v[16:31], a[96:99], v[164:167], v[16:31]
	ds_read_b128 v[164:167], v192 offset:58368
	v_exp_f32_e32 v209, v121
	v_add_f32_e32 v201, 1.0, v201
	v_add_f32_e32 v202, 1.0, v202
	v_mfma_f32_32x32x16_f16 v[0:15], a[100:103], v[168:171], v[0:15]
	ds_read_b128 v[168:171], v192 offset:59392
	v_exp_f32_e32 v210, v122
	v_add_f32_e32 v203, 1.0, v203
	v_add_f32_e32 v204, 1.0, v204
	v_mfma_f32_32x32x16_f16 v[16:31], a[100:103], v[172:175], v[16:31]
	ds_read_b128 v[172:175], v192 offset:60416
	global_load_lds_dwordx4 v192, s[44:45] offset:1024 sc1
	v_exp_f32_e32 v211, v123
	v_add_f32_e32 v205, 1.0, v205
	v_add_f32_e32 v206, 1.0, v206
	v_mfma_f32_32x32x16_f16 v[0:15], a[104:107], v[176:179], v[0:15]
	ds_read_b128 v[176:179], v192 offset:61440
	v_exp_f32_e32 v212, v124
	v_add_f32_e32 v207, 1.0, v207
	v_add_f32_e32 v208, 1.0, v208
	v_mfma_f32_32x32x16_f16 v[16:31], a[104:107], v[180:183], v[16:31]
	ds_read_b128 v[180:183], v192 offset:62464
	v_exp_f32_e32 v213, v125
	v_add_f32_e32 v209, 1.0, v209
	v_add_f32_e32 v210, 1.0, v210
	s_waitcnt lgkmcnt(2)
	v_mfma_f32_32x32x16_f16 v[0:15], a[108:111], v[184:187], v[0:15]
	ds_read_b128 v[184:187], v192 offset:63488
	v_exp_f32_e32 v214, v126
	v_add_f32_e32 v211, 1.0, v211
	v_add_f32_e32 v212, 1.0, v212
	v_mfma_f32_32x32x16_f16 v[16:31], a[108:111], v[188:191], v[16:31]
	ds_read_b128 v[188:191], v192 offset:64512
	global_load_lds_dwordx4 v192, s[44:45] offset:2048 sc1
	v_exp_f32_e32 v215, v127
	v_add_f32_e32 v213, 1.0, v213
	v_add_f32_e32 v214, 1.0, v214
	s_waitcnt vmcnt(7)
	s_barrier
	v_mfma_f32_32x32x16_f16 v[0:15], a[112:115], v[160:163], v[0:15]
	ds_read_b128 v[160:163], v193 offset:0
	v_add_f32_e32 v215, 1.0, v215
	v_rcp_f32_e32 v200, v200
	v_mfma_f32_32x32x16_f16 v[16:31], a[112:115], v[164:167], v[16:31]
	ds_read_b128 v[164:167], v193 offset:1024
	v_rcp_f32_e32 v201, v201
	v_mfma_f32_32x32x16_f16 v[0:15], a[116:119], v[168:171], v[0:15]
	ds_read_b128 v[168:171], v193 offset:2048
	v_rcp_f32_e32 v202, v202
	v_mfma_f32_32x32x16_f16 v[16:31], a[116:119], v[172:175], v[16:31]
	ds_read_b128 v[172:175], v193 offset:3072
	global_load_lds_dwordx4 v192, s[44:45] offset:3072 sc1
	v_rcp_f32_e32 v203, v203
	s_waitcnt lgkmcnt(2)
	v_mfma_f32_32x32x16_f16 v[0:15], a[120:123], v[176:179], v[0:15]
	ds_read_b128 v[176:179], v193 offset:4096
	v_rcp_f32_e32 v204, v204
	v_mfma_f32_32x32x16_f16 v[16:31], a[120:123], v[180:183], v[16:31]
	ds_read_b128 v[180:183], v193 offset:5120
	v_rcp_f32_e32 v205, v205
	v_mul_f32_e32 v204, v204, v156
	v_mfma_f32_32x32x16_f16 v[0:15], a[124:127], v[184:187], v[0:15]
	ds_read_b128 v[184:187], v193 offset:6144
	v_rcp_f32_e32 v206, v206
	v_mul_f32_e32 v205, v205, v157
	v_mfma_f32_32x32x16_f16 v[16:31], a[124:127], v[188:191], v[16:31]
	ds_read_b128 v[188:191], v193 offset:7168
	v_cmp_gt_u32_e32 vcc, 2, v251
	s_cbranch_vccnz .LD_tpoll17
.LD_tok16:
	s_and_b32 s64, s71, 1
	s_lshl_b32 s64, s64, 22
	s_add_u32 s64, s64, s49
	s_add_u32 s64, s64, 0x20000
	s_add_u32 s34, s6, s64
	s_addc_u32 s35, s7, 0
	s_mov_b32 m0, s52
	s_add_u32 s44, s34, 0x0
	s_addc_u32 s45, s35, 0
	global_load_lds_dwordx4 v192, s[44:45] sc1
	v_rcp_f32_e32 v207, v207
	v_mul_f32_e32 v206, v206, v158
	v_mfma_f32_32x32x16_f16 v[0:15], a[128:131], v[160:163], v[0:15]
	ds_read_b128 v[160:163], v193 offset:8192
	v_rcp_f32_e32 v208, v208
	v_mul_f32_e32 v207, v207, v159
	v_mfma_f32_32x32x16_f16 v[16:31], a[128:131], v[164:167], v[16:31]
	ds_read_b128 v[164:167], v193 offset:9216
	v_rcp_f32_e32 v209, v209
	v_fmamk_f32 v208, v208, 0xc0b8aa3b, v198
	s_waitcnt lgkmcnt(2)
	v_mfma_f32_32x32x16_f16 v[0:15], a[132:135], v[168:171], v[0:15]
	ds_read_b128 v[168:171], v193 offset:10240
	v_rcp_f32_e32 v210, v210
	v_fmamk_f32 v209, v209, 0xc0b8aa3b, v198
	v_fma_f32 v156, v200, v208, v204
	s_add_u32 s46, s42, 0x4000
	s_addc_u32 s47, s43, 0
	global_load_dwordx4 v[64:67], v192, s[46:47] offset:0
	v_mfma_f32_32x32x16_f16 v[16:31], a[132:135], v[172:175], v[16:31]
	ds_read_b128 v[172:175], v193 offset:11264
	global_load_lds_dwordx4 v192, s[44:45] offset:1024 sc1
	v_rcp_f32_e32 v211, v211
	v_fmamk_f32 v210, v210, 0xc0b8aa3b, v198
	v_fma_f32 v157, v201, v209, v205
	global_load_dwordx4 v[68:71], v192, s[46:47] offset:1024
	global_load_dwordx4 v[72:75], v192, s[46:47] offset:2048
	v_mfma_f32_32x32x16_f16 v[0:15], a[136:139], v[176:179], v[0:15]
	ds_read_b128 v[176:179], v193 offset:12288
	v_rcp_f32_e32 v212, v212
	v_fmamk_f32 v211, v211, 0xc0b8aa3b, v198
	v_fma_f32 v158, v202, v210, v206
	global_load_dwordx4 v[76:79], v192, s[46:47] offset:3072
	s_add_u32 s46, s42, 0x5000
	s_addc_u32 s47, s43, 0
	v_mfma_f32_32x32x16_f16 v[16:31], a[136:139], v[180:183], v[16:31]
	ds_read_b128 v[180:183], v193 offset:13312
	v_rcp_f32_e32 v213, v213
	v_fma_f32 v159, v203, v211, v207
	global_load_dwordx4 v[80:83], v192, s[46:47] offset:0
	global_load_dwordx4 v[84:87], v192, s[46:47] offset:1024
	v_mfma_f32_32x32x16_f16 v[0:15], a[140:143], v[184:187], v[0:15]
	ds_read_b128 v[184:187], v193 offset:14336
	v_rcp_f32_e32 v214, v214
	global_load_dwordx4 v[88:91], v192, s[46:47] offset:2048
	global_load_dwordx4 v[92:95], v192, s[46:47] offset:3072
	v_mfma_f32_32x32x16_f16 v[16:31], a[140:143], v[188:191], v[16:31]
	ds_read_b128 v[188:191], v193 offset:15360
	global_load_lds_dwordx4 v192, s[44:45] offset:2048 sc1
	v_rcp_f32_e32 v215, v215
	s_waitcnt lgkmcnt(2)
	v_mfma_f32_32x32x16_f16 v[0:15], a[144:147], v[160:163], v[0:15]
	ds_read_b128 v[160:163], v193 offset:16384
	v_exp_f32_e32 v200, v156
	v_mfma_f32_32x32x16_f16 v[16:31], a[144:147], v[164:167], v[16:31]
	ds_read_b128 v[164:167], v193 offset:17408
	v_exp_f32_e32 v201, v157
	v_add_f32_e32 v200, 1.0, v200
	v_mfma_f32_32x32x16_f16 v[0:15], a[148:151], v[168:171], v[0:15]
	ds_read_b128 v[168:171], v193 offset:18432
	v_exp_f32_e32 v202, v158
	v_add_f32_e32 v201, 1.0, v201
	v_mfma_f32_32x32x16_f16 v[16:31], a[148:151], v[172:175], v[16:31]
	ds_read_b128 v[172:175], v193 offset:19456
	global_load_lds_dwordx4 v192, s[44:45] offset:3072 sc1
	v_exp_f32_e32 v203, v159
	v_add_f32_e32 v202, 1.0, v202
	v_mfma_f32_32x32x16_f16 v[0:15], a[152:155], v[176:179], v[0:15]
	ds_read_b128 v[176:179], v193 offset:20480
	v_add_f32_e32 v203, 1.0, v203
	v_rcp_f32_e32 v200, v200
	v_mfma_f32_32x32x16_f16 v[16:31], a[152:155], v[180:183], v[16:31]
	ds_read_b128 v[180:183], v193 offset:21504
	v_rcp_f32_e32 v201, v201
	v_fma_f32 v200, v200, 2.0, -1.0
	s_waitcnt lgkmcnt(2)
	v_mfma_f32_32x32x16_f16 v[0:15], a[156:159], v[184:187], v[0:15]
	ds_read_b128 v[184:187], v193 offset:22528
	v_rcp_f32_e32 v202, v202
	v_fma_f32 v201, v201, 2.0, -1.0
	v_mul_f32_e32 v216, v212, v200
	v_mfma_f32_32x32x16_f16 v[16:31], a[156:159], v[188:191], v[16:31]
	ds_read_b128 v[188:191], v193 offset:23552
	s_mov_b32 m0, s53
	s_add_u32 s44, s34, 0x1000
	s_addc_u32 s45, s35, 0
	global_load_lds_dwordx4 v192, s[44:45] sc1
	v_rcp_f32_e32 v203, v203
	v_fma_f32 v202, v202, 2.0, -1.0
	v_mul_f32_e32 v217, v213, v201
	v_mfma_f32_32x32x16_f16 v[0:15], a[160:163], v[160:163], v[0:15]
	ds_read_b128 v[160:163], v193 offset:24576
	v_fma_f32 v203, v203, 2.0, -1.0
	v_mul_f32_e32 v218, v214, v202
	v_mfma_f32_32x32x16_f16 v[16:31], a[160:163], v[164:167], v[16:31]
	ds_read_b128 v[164:167], v193 offset:25600
	v_mul_f32_e32 v219, v215, v203
	v_mul_f32_e32 v236, v216, v228
	v_mfma_f32_32x32x16_f16 v[0:15], a[164:167], v[168:171], v[0:15]
	ds_read_b128 v[168:171], v193 offset:26624
	v_mul_f32_e32 v237, v216, v232
	v_fmac_f32_e32 v236, v217, v229
	v_mfma_f32_32x32x16_f16 v[16:31], a[164:167], v[172:175], v[16:31]
	ds_read_b128 v[172:175], v193 offset:27648
	global_load_lds_dwordx4 v192, s[44:45] offset:1024 sc1
	v_fmac_f32_e32 v237, v217, v233
	v_fmac_f32_e32 v236, v218, v230
	s_waitcnt lgkmcnt(2)
	v_mfma_f32_32x32x16_f16 v[0:15], a[168:171], v[176:179], v[0:15]
	ds_read_b128 v[176:179], v193 offset:28672
	v_fmac_f32_e32 v237, v218, v234
	v_fmac_f32_e32 v236, v219, v231
	v_mfma_f32_32x32x16_f16 v[16:31], a[168:171], v[180:183], v[16:31]
	ds_read_b128 v[180:183], v193 offset:29696
	v_fmac_f32_e32 v237, v219, v235
	v_mov_b32_e32 v238, v236
	v_mfma_f32_32x32x16_f16 v[0:15], a[172:175], v[184:187], v[0:15]
	ds_read_b128 v[184:187], v193 offset:30720
	v_mov_b32_e32 v240, v237
	v_cvt_pk_f16_f32 v222, v216, v217
	v_mfma_f32_32x32x16_f16 v[16:31], a[172:175], v[188:191], v[16:31]
	ds_read_b128 v[188:191], v193 offset:31744
	global_load_lds_dwordx4 v192, s[44:45] offset:2048 sc1
	v_permlane32_swap_b32_e32 v236, v238
	v_permlane32_swap_b32_e32 v237, v240
	v_add_f32_e32 v238, v236, v238
	v_add_f32_e32 v239, v237, v240
	ds_write_b64 v248, v[238:239] offset:1792
	s_waitcnt vmcnt(15)
	s_barrier
	v_mfma_f32_32x32x16_f16 v[0:15], a[176:179], v[160:163], v[0:15]
	ds_read_b128 v[160:163], v193 offset:32768
	v_cvt_pk_f16_f32 v223, v218, v219
	v_mfma_f32_32x32x16_f16 v[16:31], a[176:179], v[164:167], v[16:31]
	ds_read_b128 v[164:167], v193 offset:33792
	v_permlane32_swap_b32_e32 v220, v222
	v_permlane32_swap_b32_e32 v221, v223
	s_cmp_eq_u32 s31, 0
	s_cbranch_scc1 .LD_slow18
	global_store_dwordx4 v195, v[220:223], s[36:37] offset:0

.LD_join21:
	ds_read_b64 v[200:201], v249 offset:1536
	ds_read_b64 v[202:203], v249 offset:3584
	ds_read_b64 v[204:205], v249 offset:5632
	ds_read_b64 v[206:207], v249 offset:7680
	v_mfma_f32_32x32x16_f16 v[16:31], a[212:215], v[172:175], v[16:31]
	ds_read_b128 v[172:175], v193 offset:52224
	global_load_lds_dwordx4 v192, s[44:45] offset:3072 sc1
	s_waitcnt lgkmcnt(6)
	v_mfma_f32_32x32x16_f16 v[0:15], a[216:219], v[176:179], v[0:15]
	ds_read_b128 v[176:179], v193 offset:53248
	v_mfma_f32_32x32x16_f16 v[16:31], a[216:219], v[180:183], v[16:31]
	ds_read_b128 v[180:183], v193 offset:54272
	v_mfma_f32_32x32x16_f16 v[0:15], a[220:223], v[184:187], v[0:15]
	ds_read_b128 v[184:187], v193 offset:55296
	v_mfma_f32_32x32x16_f16 v[16:31], a[220:223], v[188:191], v[16:31]
	ds_read_b128 v[188:191], v193 offset:56320
	s_mov_b32 m0, s55
	s_add_u32 s44, s34, 0x9000
	s_addc_u32 s45, s35, 0
	global_load_lds_dwordx4 v192, s[44:45] sc1
	v_mfma_f32_32x32x16_f16 v[0:15], a[224:227], v[160:163], v[0:15]
	ds_read_b128 v[160:163], v193 offset:57344
	v_mfma_f32_32x32x16_f16 v[16:31], a[224:227], v[164:167], v[16:31]
	ds_read_b128 v[164:167], v193 offset:58368
	s_waitcnt lgkmcnt(2)
	v_mfma_f32_32x32x16_f16 v[0:15], a[228:231], v[168:171], v[0:15]
	ds_read_b128 v[168:171], v193 offset:59392
	v_mfma_f32_32x32x16_f16 v[16:31], a[228:231], v[172:175], v[16:31]
	ds_read_b128 v[172:175], v193 offset:60416
	global_load_lds_dwordx4 v192, s[44:45] offset:1024 sc1
	v_mfma_f32_32x32x16_f16 v[0:15], a[232:235], v[176:179], v[0:15]
	ds_read_b128 v[176:179], v193 offset:61440
	v_mfma_f32_32x32x16_f16 v[16:31], a[232:235], v[180:183], v[16:31]
	ds_read_b128 v[180:183], v193 offset:62464
	v_mfma_f32_32x32x16_f16 v[0:15], a[236:239], v[184:187], v[0:15]
	ds_read_b128 v[184:187], v193 offset:63488
	v_add_f32_e32 v200, v200, v202
	v_add_f32_e32 v201, v201, v203
	v_add_f32_e32 v200, v200, v204
	v_add_f32_e32 v201, v201, v205
	v_add_f32_e32 v200, v200, v206
	v_add_f32_e32 v201, v201, v207
	global_store_dwordx2 v250, v[200:201], s[72:73]
	v_mfma_f32_32x32x16_f16 v[16:31], a[236:239], v[188:191], v[16:31]
	ds_read_b128 v[188:191], v193 offset:64512
	global_load_lds_dwordx4 v192, s[44:45] offset:2048 sc1
	s_waitcnt vmcnt(9)
	s_barrier
	s_waitcnt lgkmcnt(2)
	v_mfma_f32_32x32x16_f16 v[0:15], a[240:243], v[160:163], v[0:15]
	ds_read_b128 v[160:163], v192 offset:0
	v_mfma_f32_32x32x16_f16 v[16:31], a[240:243], v[164:167], v[16:31]
	ds_read_b128 v[164:167], v192 offset:1024
	v_mfma_f32_32x32x16_f16 v[0:15], a[244:247], v[168:171], v[0:15]
	ds_read_b128 v[168:171], v192 offset:2048
	s_and_b32 s64, s33, 1
	s_lshl_b32 s64, s64, 22
	s_add_u32 s64, s64, s50
	s_add_u32 s36, s6, s64
	s_addc_u32 s37, s7, 0
	s_lshl_b32 s64, s33, 3
	s_add_u32 s64, s64, s29
	s_lshl_b32 s64, s64, 5
	s_add_u32 s64, s64, s30
	s_lshl_b32 s64, s64, 2
	s_add_u32 s40, s8, s64
	s_addc_u32 s41, s9, 0
	s_lshl_b32 s64, s33, 19
	s_add_u32 s72, s62, s64
	s_addc_u32 s73, s63, 0
	v_mfma_f32_32x32x16_f16 v[16:31], a[244:247], v[172:175], v[16:31]
	ds_read_b128 v[172:175], v192 offset:3072
	global_load_lds_dwordx4 v192, s[44:45] offset:3072 sc1
	v_mfma_f32_32x32x16_f16 v[0:15], a[248:251], v[176:179], v[0:15]
	ds_read_b128 v[176:179], v192 offset:4096
	v_mfma_f32_32x32x16_f16 v[16:31], a[248:251], v[180:183], v[16:31]
	ds_read_b128 v[180:183], v192 offset:5120
	s_waitcnt lgkmcnt(2)
	v_mfma_f32_32x32x16_f16 v[0:15], a[252:255], v[184:187], v[0:15]
	ds_read_b128 v[184:187], v192 offset:6144
	v_mfma_f32_32x32x16_f16 v[16:31], a[252:255], v[188:191], v[16:31]
	ds_read_b128 v[188:191], v192 offset:7168
	s_mov_b32 m0, s56
	s_add_u32 s44, s34, 0x10000
	s_addc_u32 s45, s35, 0
	global_load_lds_dwordx4 v192, s[44:45] sc1
	s_nop 3
	s_waitcnt lgkmcnt(2)
	v_mfma_f32_32x32x16_f16 v[32:47], a[0:3], v[160:163], v[32:47]
	ds_read_b128 v[160:163], v192 offset:8192
	v_exp_f32_e32 v200, v0
	v_mfma_f32_32x32x16_f16 v[48:63], a[0:3], v[164:167], v[48:63]
	ds_read_b128 v[164:167], v192 offset:9216
	s_lshl_b32 s64, s71, 3
	s_add_u32 s64, s64, s29
	s_lshl_b32 s64, s64, 7
	s_add_u32 s38, s8, s64
	s_addc_u32 s39, s9, 0
	global_load_dword v251, v196, s[38:39] sc1
	v_exp_f32_e32 v201, v1
	v_add_f32_e32 v200, 1.0, v200
	v_mfma_f32_32x32x16_f16 v[32:47], a[4:7], v[168:171], v[32:47]
	ds_read_b128 v[168:171], v192 offset:10240
	v_exp_f32_e32 v202, v2
	v_add_f32_e32 v201, 1.0, v201
	v_mfma_f32_32x32x16_f16 v[48:63], a[4:7], v[172:175], v[48:63]
	ds_read_b128 v[172:175], v192 offset:11264
	global_load_lds_dwordx4 v192, s[44:45] offset:1024 sc1
	v_exp_f32_e32 v203, v3
	v_add_f32_e32 v202, 1.0, v202
	v_mfma_f32_32x32x16_f16 v[32:47], a[8:11], v[176:179], v[32:47]
	ds_read_b128 v[176:179], v192 offset:12288
	v_exp_f32_e32 v204, v4
	v_add_f32_e32 v203, 1.0, v203
	v_mfma_f32_32x32x16_f16 v[48:63], a[8:11], v[180:183], v[48:63]
	ds_read_b128 v[180:183], v192 offset:13312
	v_exp_f32_e32 v205, v5
	v_add_f32_e32 v204, 1.0, v204
	s_waitcnt lgkmcnt(2)
	v_mfma_f32_32x32x16_f16 v[32:47], a[12:15], v[184:187], v[32:47]
	ds_read_b128 v[184:187], v192 offset:14336
	v_exp_f32_e32 v206, v6
	v_add_f32_e32 v205, 1.0, v205
	v_mfma_f32_32x32x16_f16 v[48:63], a[12:15], v[188:191], v[48:63]
	ds_read_b128 v[188:191], v192 offset:15360
	global_load_lds_dwordx4 v192, s[44:45] offset:2048 sc1
	v_exp_f32_e32 v207, v7
	v_add_f32_e32 v206, 1.0, v206
	v_mfma_f32_32x32x16_f16 v[32:47], a[16:19], v[160:163], v[32:47]
	ds_read_b128 v[160:163], v192 offset:16384
	v_exp_f32_e32 v208, v8
	v_add_f32_e32 v207, 1.0, v207
	v_mfma_f32_32x32x16_f16 v[48:63], a[16:19], v[164:167], v[48:63]
	ds_read_b128 v[164:167], v192 offset:17408
	v_exp_f32_e32 v209, v9
	v_add_f32_e32 v208, 1.0, v208
	v_mfma_f32_32x32x16_f16 v[32:47], a[20:23], v[168:171], v[32:47]
	ds_read_b128 v[168:171], v192 offset:18432
	v_exp_f32_e32 v210, v10
	v_add_f32_e32 v209, 1.0, v209
	v_mfma_f32_32x32x16_f16 v[48:63], a[20:23], v[172:175], v[48:63]
	ds_read_b128 v[172:175], v192 offset:19456
	global_load_lds_dwordx4 v192, s[44:45] offset:3072 sc1
	v_exp_f32_e32 v211, v11
	v_add_f32_e32 v210, 1.0, v210
	s_waitcnt lgkmcnt(2)
	v_mfma_f32_32x32x16_f16 v[32:47], a[24:27], v[176:179], v[32:47]
	ds_read_b128 v[176:179], v192 offset:20480
	v_exp_f32_e32 v212, v12
	v_add_f32_e32 v211, 1.0, v211
	v_mfma_f32_32x32x16_f16 v[48:63], a[24:27], v[180:183], v[48:63]
	ds_read_b128 v[180:183], v192 offset:21504
	v_exp_f32_e32 v213, v13
	v_add_f32_e32 v212, 1.0, v212
	v_mfma_f32_32x32x16_f16 v[32:47], a[28:31], v[184:187], v[32:47]
	ds_read_b128 v[184:187], v192 offset:22528
	v_exp_f32_e32 v214, v14
	v_add_f32_e32 v213, 1.0, v213
	v_mfma_f32_32x32x16_f16 v[48:63], a[28:31], v[188:191], v[48:63]
	ds_read_b128 v[188:191], v192 offset:23552
	s_mov_b32 m0, s57
	s_add_u32 s44, s34, 0x11000
	s_addc_u32 s45, s35, 0
	global_load_lds_dwordx4 v192, s[44:45] sc1
	v_exp_f32_e32 v215, v15
	v_add_f32_e32 v214, 1.0, v214
	v_mfma_f32_32x32x16_f16 v[32:47], a[32:35], v[160:163], v[32:47]
	ds_read_b128 v[160:163], v192 offset:24576
	v_add_f32_e32 v215, 1.0, v215
	v_rcp_f32_e32 v200, v200
	v_mfma_f32_32x32x16_f16 v[48:63], a[32:35], v[164:167], v[48:63]
	ds_read_b128 v[164:167], v192 offset:25600
	v_rcp_f32_e32 v201, v201
	s_waitcnt lgkmcnt(2)
	v_mfma_f32_32x32x16_f16 v[32:47], a[36:39], v[168:171], v[32:47]
	ds_read_b128 v[168:171], v192 offset:26624
	v_rcp_f32_e32 v202, v202
	v_mfma_f32_32x32x16_f16 v[48:63], a[36:39], v[172:175], v[48:63]
	ds_read_b128 v[172:175], v192 offset:27648
	global_load_lds_dwordx4 v192, s[44:45] offset:1024 sc1
	v_rcp_f32_e32 v203, v203
	v_mfma_f32_32x32x16_f16 v[32:47], a[40:43], v[176:179], v[32:47]
	ds_read_b128 v[176:179], v192 offset:28672
	v_rcp_f32_e32 v204, v204
	v_mfma_f32_32x32x16_f16 v[48:63], a[40:43], v[180:183], v[48:63]
	ds_read_b128 v[180:183], v192 offset:29696
	v_rcp_f32_e32 v205, v205
	v_mul_f32_e32 v204, v204, v128
	v_mfma_f32_32x32x16_f16 v[32:47], a[44:47], v[184:187], v[32:47]
	ds_read_b128 v[184:187], v192 offset:30720
	v_rcp_f32_e32 v206, v206
	v_mul_f32_e32 v205, v205, v129
	v_mfma_f32_32x32x16_f16 v[48:63], a[44:47], v[188:191], v[48:63]
	ds_read_b128 v[188:191], v192 offset:31744
	global_load_lds_dwordx4 v192, s[44:45] offset:2048 sc1
	v_rcp_f32_e32 v207, v207
	v_mul_f32_e32 v206, v206, v130
	s_waitcnt vmcnt(8)
	s_barrier
	s_waitcnt lgkmcnt(2)
	v_mfma_f32_32x32x16_f16 v[32:47], a[48:51], v[160:163], v[32:47]
	ds_read_b128 v[160:163], v192 offset:32768
	v_rcp_f32_e32 v208, v208
	v_mul_f32_e32 v207, v207, v131
	v_mfma_f32_32x32x16_f16 v[48:63], a[48:51], v[164:167], v[48:63]
	ds_read_b128 v[164:167], v192 offset:33792
	v_rcp_f32_e32 v209, v209
	v_fmamk_f32 v208, v208, 0xc0b8aa3b, v198
	v_mfma_f32_32x32x16_f16 v[32:47], a[52:55], v[168:171], v[32:47]
	ds_read_b128 v[168:171], v192 offset:34816
	v_rcp_f32_e32 v210, v210
	v_fmamk_f32 v209, v209, 0xc0b8aa3b, v198
	v_fma_f32 v128, v200, v208, v204
	v_mfma_f32_32x32x16_f16 v[48:63], a[52:55], v[172:175], v[48:63]
	ds_read_b128 v[172:175], v192 offset:35840
	global_load_lds_dwordx4 v192, s[44:45] offset:3072 sc1
	v_rcp_f32_e32 v211, v211
	v_fmamk_f32 v210, v210, 0xc0b8aa3b, v198
	v_fma_f32 v129, v201, v209, v205
	v_mfma_f32_32x32x16_f16 v[32:47], a[56:59], v[176:179], v[32:47]
	ds_read_b128 v[176:179], v192 offset:36864
	v_rcp_f32_e32 v212, v212
	v_fmamk_f32 v211, v211, 0xc0b8aa3b, v198
	v_fma_f32 v130, v202, v210, v206
	v_mfma_f32_32x32x16_f16 v[48:63], a[56:59], v[180:183], v[48:63]
	ds_read_b128 v[180:183], v192 offset:37888
	v_rcp_f32_e32 v213, v213
	v_fma_f32 v131, v203, v211, v207
	s_waitcnt lgkmcnt(2)
	v_mfma_f32_32x32x16_f16 v[32:47], a[60:63], v[184:187], v[32:47]
	ds_read_b128 v[184:187], v192 offset:38912
	v_rcp_f32_e32 v214, v214
	v_mfma_f32_32x32x16_f16 v[48:63], a[60:63], v[188:191], v[48:63]
	ds_read_b128 v[188:191], v192 offset:39936
	s_mov_b32 m0, s58
	s_add_u32 s44, s34, 0x18000
	s_addc_u32 s45, s35, 0
	global_load_lds_dwordx4 v192, s[44:45] sc1
	v_rcp_f32_e32 v215, v215
	v_mfma_f32_32x32x16_f16 v[32:47], a[64:67], v[160:163], v[32:47]
	ds_read_b128 v[160:163], v192 offset:40960
	v_exp_f32_e32 v200, v128
	v_mfma_f32_32x32x16_f16 v[48:63], a[64:67], v[164:167], v[48:63]
	ds_read_b128 v[164:167], v192 offset:41984
	v_exp_f32_e32 v201, v129
	v_add_f32_e32 v200, 1.0, v200
	v_mfma_f32_32x32x16_f16 v[32:47], a[68:71], v[168:171], v[32:47]
	ds_read_b128 v[168:171], v192 offset:43008
	v_exp_f32_e32 v202, v130
	v_add_f32_e32 v201, 1.0, v201
	v_mfma_f32_32x32x16_f16 v[48:63], a[68:71], v[172:175], v[48:63]
	ds_read_b128 v[172:175], v192 offset:44032
	global_load_lds_dwordx4 v192, s[44:45] offset:1024 sc1
	v_exp_f32_e32 v203, v131
	v_add_f32_e32 v202, 1.0, v202
	s_waitcnt lgkmcnt(2)
	v_mfma_f32_32x32x16_f16 v[32:47], a[72:75], v[176:179], v[32:47]
	ds_read_b128 v[176:179], v192 offset:45056
	v_add_f32_e32 v203, 1.0, v203
	v_rcp_f32_e32 v200, v200
	v_mfma_f32_32x32x16_f16 v[48:63], a[72:75], v[180:183], v[48:63]
	ds_read_b128 v[180:183], v192 offset:46080
	v_rcp_f32_e32 v201, v201
	v_fma_f32 v200, v200, 2.0, -1.0
	v_mfma_f32_32x32x16_f16 v[32:47], a[76:79], v[184:187], v[32:47]
	ds_read_b128 v[184:187], v192 offset:47104
	v_rcp_f32_e32 v202, v202
	v_fma_f32 v201, v201, 2.0, -1.0
	v_mul_f32_e32 v216, v212, v200
	v_mfma_f32_32x32x16_f16 v[48:63], a[76:79], v[188:191], v[48:63]
	ds_read_b128 v[188:191], v192 offset:48128
	global_load_lds_dwordx4 v192, s[44:45] offset:2048 sc1
	v_rcp_f32_e32 v203, v203
	v_fma_f32 v202, v202, 2.0, -1.0
	v_mul_f32_e32 v217, v213, v201
	v_mfma_f32_32x32x16_f16 v[32:47], a[80:83], v[160:163], v[32:47]
	ds_read_b128 v[160:163], v192 offset:49152
	v_fma_f32 v203, v203, 2.0, -1.0
	v_mul_f32_e32 v218, v214, v202
	v_exp_f32_e32 v200, v16
	v_mfma_f32_32x32x16_f16 v[48:63], a[80:83], v[164:167], v[48:63]
	ds_read_b128 v[164:167], v192 offset:50176
	v_mul_f32_e32 v219, v215, v203
	v_mul_f32_e32 v236, v216, v228
	v_exp_f32_e32 v201, v17
	s_waitcnt lgkmcnt(2)
	v_mfma_f32_32x32x16_f16 v[32:47], a[84:87], v[168:171], v[32:47]
	ds_read_b128 v[168:171], v192 offset:51200
	v_mul_f32_e32 v237, v216, v232
	v_fmac_f32_e32 v236, v217, v229
	v_exp_f32_e32 v202, v18
	v_mfma_f32_32x32x16_f16 v[48:63], a[84:87], v[172:175], v[48:63]
	ds_read_b128 v[172:175], v192 offset:52224
	global_load_lds_dwordx4 v192, s[44:45] offset:3072 sc1
	v_fmac_f32_e32 v237, v217, v233
	v_fmac_f32_e32 v236, v218, v230
	v_exp_f32_e32 v203, v19
	v_mfma_f32_32x32x16_f16 v[32:47], a[88:91], v[176:179], v[32:47]
	ds_read_b128 v[176:179], v192 offset:53248
	v_fmac_f32_e32 v237, v218, v234
	v_fmac_f32_e32 v236, v219, v231
	v_exp_f32_e32 v204, v20
	v_mfma_f32_32x32x16_f16 v[48:63], a[88:91], v[180:183], v[48:63]
	ds_read_b128 v[180:183], v192 offset:54272
	v_fmac_f32_e32 v237, v219, v235
	v_mov_b32_e32 v238, v236
	v_exp_f32_e32 v205, v21
	v_mfma_f32_32x32x16_f16 v[32:47], a[92:95], v[184:187], v[32:47]
	ds_read_b128 v[184:187], v192 offset:55296
	v_mov_b32_e32 v240, v237
	v_cvt_pk_f16_f32 v220, v216, v217
	v_exp_f32_e32 v206, v22
	v_mfma_f32_32x32x16_f16 v[48:63], a[92:95], v[188:191], v[48:63]
	ds_read_b128 v[188:191], v192 offset:56320
	s_mov_b32 m0, s59
	s_add_u32 s44, s34, 0x19000
	s_addc_u32 s45, s35, 0
	global_load_lds_dwordx4 v192, s[44:45] sc1
	v_permlane32_swap_b32_e32 v236, v238
	v_permlane32_swap_b32_e32 v237, v240
	v_add_f32_e32 v238, v236, v238
	v_add_f32_e32 v239, v237, v240
	ds_write_b64 v248, v[238:239] offset:0
	v_exp_f32_e32 v207, v23
	s_waitcnt lgkmcnt(3)
	v_mfma_f32_32x32x16_f16 v[32:47], a[96:99], v[160:163], v[32:47]
	ds_read_b128 v[160:163], v192 offset:57344
	v_cvt_pk_f16_f32 v221, v218, v219
	v_exp_f32_e32 v208, v24
	v_add_f32_e32 v200, 1.0, v200
	v_mfma_f32_32x32x16_f16 v[48:63], a[96:99], v[164:167], v[48:63]
	ds_read_b128 v[164:167], v192 offset:58368
	v_exp_f32_e32 v209, v25
	v_add_f32_e32 v201, 1.0, v201
	v_add_f32_e32 v202, 1.0, v202
	v_mfma_f32_32x32x16_f16 v[32:47], a[100:103], v[168:171], v[32:47]
	ds_read_b128 v[168:171], v192 offset:59392
	v_exp_f32_e32 v210, v26
	v_add_f32_e32 v203, 1.0, v203
	v_add_f32_e32 v204, 1.0, v204
	v_mfma_f32_32x32x16_f16 v[48:63], a[100:103], v[172:175], v[48:63]
	ds_read_b128 v[172:175], v192 offset:60416
	global_load_lds_dwordx4 v192, s[44:45] offset:1024 sc1
	v_exp_f32_e32 v211, v27
	v_add_f32_e32 v205, 1.0, v205
	v_add_f32_e32 v206, 1.0, v206
	v_mfma_f32_32x32x16_f16 v[32:47], a[104:107], v[176:179], v[32:47]
	ds_read_b128 v[176:179], v192 offset:61440
	v_exp_f32_e32 v212, v28
	v_add_f32_e32 v207, 1.0, v207
	v_add_f32_e32 v208, 1.0, v208
	v_mfma_f32_32x32x16_f16 v[48:63], a[104:107], v[180:183], v[48:63]
	ds_read_b128 v[180:183], v192 offset:62464
	v_exp_f32_e32 v213, v29
	v_add_f32_e32 v209, 1.0, v209
	v_add_f32_e32 v210, 1.0, v210
	s_waitcnt lgkmcnt(2)
	v_mfma_f32_32x32x16_f16 v[32:47], a[108:111], v[184:187], v[32:47]
	ds_read_b128 v[184:187], v192 offset:63488
	v_exp_f32_e32 v214, v30
	v_add_f32_e32 v211, 1.0, v211
	v_add_f32_e32 v212, 1.0, v212
	v_mfma_f32_32x32x16_f16 v[48:63], a[108:111], v[188:191], v[48:63]
	ds_read_b128 v[188:191], v192 offset:64512
	global_load_lds_dwordx4 v192, s[44:45] offset:2048 sc1
	v_exp_f32_e32 v215, v31
	v_add_f32_e32 v213, 1.0, v213
	v_add_f32_e32 v214, 1.0, v214
	s_waitcnt vmcnt(7)
	s_barrier
	v_mfma_f32_32x32x16_f16 v[32:47], a[112:115], v[160:163], v[32:47]
	ds_read_b128 v[160:163], v193 offset:0
	v_add_f32_e32 v215, 1.0, v215
	v_rcp_f32_e32 v200, v200
	v_mfma_f32_32x32x16_f16 v[48:63], a[112:115], v[164:167], v[48:63]
	ds_read_b128 v[164:167], v193 offset:1024
	v_rcp_f32_e32 v201, v201
	v_mfma_f32_32x32x16_f16 v[32:47], a[116:119], v[168:171], v[32:47]
	ds_read_b128 v[168:171], v193 offset:2048
	v_rcp_f32_e32 v202, v202
	v_mfma_f32_32x32x16_f16 v[48:63], a[116:119], v[172:175], v[48:63]
	ds_read_b128 v[172:175], v193 offset:3072
	global_load_lds_dwordx4 v192, s[44:45] offset:3072 sc1
	v_rcp_f32_e32 v203, v203
	s_waitcnt lgkmcnt(2)
	v_mfma_f32_32x32x16_f16 v[32:47], a[120:123], v[176:179], v[32:47]
	ds_read_b128 v[176:179], v193 offset:4096
	v_rcp_f32_e32 v204, v204
	v_mfma_f32_32x32x16_f16 v[48:63], a[120:123], v[180:183], v[48:63]
	ds_read_b128 v[180:183], v193 offset:5120
	v_rcp_f32_e32 v205, v205
	v_mul_f32_e32 v204, v204, v132
	v_mfma_f32_32x32x16_f16 v[32:47], a[124:127], v[184:187], v[32:47]
	ds_read_b128 v[184:187], v193 offset:6144
	v_rcp_f32_e32 v206, v206
	v_mul_f32_e32 v205, v205, v133
	v_mfma_f32_32x32x16_f16 v[48:63], a[124:127], v[188:191], v[48:63]
	ds_read_b128 v[188:191], v193 offset:7168
	v_cmp_gt_u32_e32 vcc, 3, v251
	s_cbranch_vccnz .LD_tpoll23
.LD_tok22:
	s_and_b32 s64, s71, 1
	s_lshl_b32 s64, s64, 22
	s_add_u32 s64, s64, s49
	s_add_u32 s64, s64, 0x40000
	s_add_u32 s34, s6, s64
	s_addc_u32 s35, s7, 0
	s_mov_b32 m0, s52
	s_add_u32 s44, s34, 0x0
	s_addc_u32 s45, s35, 0
	global_load_lds_dwordx4 v192, s[44:45] sc1
	v_rcp_f32_e32 v207, v207
	v_mul_f32_e32 v206, v206, v134
	v_mfma_f32_32x32x16_f16 v[32:47], a[128:131], v[160:163], v[32:47]
	ds_read_b128 v[160:163], v193 offset:8192
	v_rcp_f32_e32 v208, v208
	v_mul_f32_e32 v207, v207, v135
	v_mfma_f32_32x32x16_f16 v[48:63], a[128:131], v[164:167], v[48:63]
	ds_read_b128 v[164:167], v193 offset:9216
	v_rcp_f32_e32 v209, v209
	v_fmamk_f32 v208, v208, 0xc0b8aa3b, v198
	s_waitcnt lgkmcnt(2)
	v_mfma_f32_32x32x16_f16 v[32:47], a[132:135], v[168:171], v[32:47]
	ds_read_b128 v[168:171], v193 offset:10240
	v_rcp_f32_e32 v210, v210
	v_fmamk_f32 v209, v209, 0xc0b8aa3b, v198
	v_fma_f32 v132, v200, v208, v204
	s_add_u32 s46, s42, 0x6000
	s_addc_u32 s47, s43, 0
	global_load_dwordx4 v[96:99], v192, s[46:47] offset:0
	v_mfma_f32_32x32x16_f16 v[48:63], a[132:135], v[172:175], v[48:63]
	ds_read_b128 v[172:175], v193 offset:11264
	global_load_lds_dwordx4 v192, s[44:45] offset:1024 sc1
	v_rcp_f32_e32 v211, v211
	v_fmamk_f32 v210, v210, 0xc0b8aa3b, v198
	v_fma_f32 v133, v201, v209, v205
	global_load_dwordx4 v[100:103], v192, s[46:47] offset:1024
	global_load_dwordx4 v[104:107], v192, s[46:47] offset:2048
	v_mfma_f32_32x32x16_f16 v[32:47], a[136:139], v[176:179], v[32:47]
	ds_read_b128 v[176:179], v193 offset:12288
	v_rcp_f32_e32 v212, v212
	v_fmamk_f32 v211, v211, 0xc0b8aa3b, v198
	v_fma_f32 v134, v202, v210, v206
	global_load_dwordx4 v[108:111], v192, s[46:47] offset:3072
	s_add_u32 s46, s42, 0x7000
	s_addc_u32 s47, s43, 0
	v_mfma_f32_32x32x16_f16 v[48:63], a[136:139], v[180:183], v[48:63]
	ds_read_b128 v[180:183], v193 offset:13312
	v_rcp_f32_e32 v213, v213
	v_fma_f32 v135, v203, v211, v207
	global_load_dwordx4 v[112:115], v192, s[46:47] offset:0
	global_load_dwordx4 v[116:119], v192, s[46:47] offset:1024
	v_mfma_f32_32x32x16_f16 v[32:47], a[140:143], v[184:187], v[32:47]
	ds_read_b128 v[184:187], v193 offset:14336
	v_rcp_f32_e32 v214, v214
	global_load_dwordx4 v[120:123], v192, s[46:47] offset:2048
	global_load_dwordx4 v[124:127], v192, s[46:47] offset:3072
	v_mfma_f32_32x32x16_f16 v[48:63], a[140:143], v[188:191], v[48:63]
	ds_read_b128 v[188:191], v193 offset:15360
	global_load_lds_dwordx4 v192, s[44:45] offset:2048 sc1
	v_rcp_f32_e32 v215, v215
	s_waitcnt lgkmcnt(2)
	v_mfma_f32_32x32x16_f16 v[32:47], a[144:147], v[160:163], v[32:47]
	ds_read_b128 v[160:163], v193 offset:16384
	v_exp_f32_e32 v200, v132
	v_mfma_f32_32x32x16_f16 v[48:63], a[144:147], v[164:167], v[48:63]
	ds_read_b128 v[164:167], v193 offset:17408
	v_exp_f32_e32 v201, v133
	v_add_f32_e32 v200, 1.0, v200
	v_mfma_f32_32x32x16_f16 v[32:47], a[148:151], v[168:171], v[32:47]
	ds_read_b128 v[168:171], v193 offset:18432
	v_exp_f32_e32 v202, v134
	v_add_f32_e32 v201, 1.0, v201
	v_mfma_f32_32x32x16_f16 v[48:63], a[148:151], v[172:175], v[48:63]
	ds_read_b128 v[172:175], v193 offset:19456
	global_load_lds_dwordx4 v192, s[44:45] offset:3072 sc1
	v_exp_f32_e32 v203, v135
	v_add_f32_e32 v202, 1.0, v202
	v_mfma_f32_32x32x16_f16 v[32:47], a[152:155], v[176:179], v[32:47]
	ds_read_b128 v[176:179], v193 offset:20480
	v_add_f32_e32 v203, 1.0, v203
	v_rcp_f32_e32 v200, v200
	v_mfma_f32_32x32x16_f16 v[48:63], a[152:155], v[180:183], v[48:63]
	ds_read_b128 v[180:183], v193 offset:21504
	v_rcp_f32_e32 v201, v201
	v_fma_f32 v200, v200, 2.0, -1.0
	s_waitcnt lgkmcnt(2)
	v_mfma_f32_32x32x16_f16 v[32:47], a[156:159], v[184:187], v[32:47]
	ds_read_b128 v[184:187], v193 offset:22528
	v_rcp_f32_e32 v202, v202
	v_fma_f32 v201, v201, 2.0, -1.0
	v_mul_f32_e32 v216, v212, v200
	v_mfma_f32_32x32x16_f16 v[48:63], a[156:159], v[188:191], v[48:63]
	ds_read_b128 v[188:191], v193 offset:23552
	s_mov_b32 m0, s53
	s_add_u32 s44, s34, 0x1000
	s_addc_u32 s45, s35, 0
	global_load_lds_dwordx4 v192, s[44:45] sc1
	v_rcp_f32_e32 v203, v203
	v_fma_f32 v202, v202, 2.0, -1.0
	v_mul_f32_e32 v217, v213, v201
	v_mfma_f32_32x32x16_f16 v[32:47], a[160:163], v[160:163], v[32:47]
	ds_read_b128 v[160:163], v193 offset:24576
	v_fma_f32 v203, v203, 2.0, -1.0
	v_mul_f32_e32 v218, v214, v202
	v_mfma_f32_32x32x16_f16 v[48:63], a[160:163], v[164:167], v[48:63]
	ds_read_b128 v[164:167], v193 offset:25600
	v_mul_f32_e32 v219, v215, v203
	v_mul_f32_e32 v236, v216, v228
	v_mfma_f32_32x32x16_f16 v[32:47], a[164:167], v[168:171], v[32:47]
	ds_read_b128 v[168:171], v193 offset:26624
	v_mul_f32_e32 v237, v216, v232
	v_fmac_f32_e32 v236, v217, v229
	v_mfma_f32_32x32x16_f16 v[48:63], a[164:167], v[172:175], v[48:63]
	ds_read_b128 v[172:175], v193 offset:27648
	global_load_lds_dwordx4 v192, s[44:45] offset:1024 sc1
	v_fmac_f32_e32 v237, v217, v233
	v_fmac_f32_e32 v236, v218, v230
	s_waitcnt lgkmcnt(2)
	v_mfma_f32_32x32x16_f16 v[32:47], a[168:171], v[176:179], v[32:47]
	ds_read_b128 v[176:179], v193 offset:28672
	v_fmac_f32_e32 v237, v218, v234
	v_fmac_f32_e32 v236, v219, v231
	v_mfma_f32_32x32x16_f16 v[48:63], a[168:171], v[180:183], v[48:63]
	ds_read_b128 v[180:183], v193 offset:29696
	v_fmac_f32_e32 v237, v219, v235
	v_mov_b32_e32 v238, v236
	v_mfma_f32_32x32x16_f16 v[32:47], a[172:175], v[184:187], v[32:47]
	ds_read_b128 v[184:187], v193 offset:30720
	v_mov_b32_e32 v240, v237
	v_cvt_pk_f16_f32 v222, v216, v217
	v_mfma_f32_32x32x16_f16 v[48:63], a[172:175], v[188:191], v[48:63]
	ds_read_b128 v[188:191], v193 offset:31744
	global_load_lds_dwordx4 v192, s[44:45] offset:2048 sc1
	v_permlane32_swap_b32_e32 v236, v238
	v_permlane32_swap_b32_e32 v237, v240
	v_add_f32_e32 v238, v236, v238
	v_add_f32_e32 v239, v237, v240
	ds_write_b64 v248, v[238:239] offset:256
	s_waitcnt vmcnt(15)
	s_barrier
	v_mfma_f32_32x32x16_f16 v[32:47], a[176:179], v[160:163], v[32:47]
	ds_read_b128 v[160:163], v193 offset:32768
	v_cvt_pk_f16_f32 v223, v218, v219
	v_mfma_f32_32x32x16_f16 v[48:63], a[176:179], v[164:167], v[48:63]
	ds_read_b128 v[164:167], v193 offset:33792
	v_permlane32_swap_b32_e32 v220, v222
	v_permlane32_swap_b32_e32 v221, v223
	s_cmp_eq_u32 s31, 0
	s_cbranch_scc1 .LD_slow24
	global_store_dwordx4 v195, v[220:223], s[36:37] offset:0

.LD_join27:
	ds_read_b64 v[200:201], v249 offset:0
	ds_read_b64 v[202:203], v249 offset:2048
	ds_read_b64 v[204:205], v249 offset:4096
	ds_read_b64 v[206:207], v249 offset:6144
	v_mfma_f32_32x32x16_f16 v[48:63], a[212:215], v[172:175], v[48:63]
	ds_read_b128 v[172:175], v193 offset:52224
	global_load_lds_dwordx4 v192, s[44:45] offset:3072 sc1
	s_waitcnt lgkmcnt(6)
	v_mfma_f32_32x32x16_f16 v[32:47], a[216:219], v[176:179], v[32:47]
	ds_read_b128 v[176:179], v193 offset:53248
	v_mfma_f32_32x32x16_f16 v[48:63], a[216:219], v[180:183], v[48:63]
	ds_read_b128 v[180:183], v193 offset:54272
	v_mfma_f32_32x32x16_f16 v[32:47], a[220:223], v[184:187], v[32:47]
	ds_read_b128 v[184:187], v193 offset:55296
	v_mfma_f32_32x32x16_f16 v[48:63], a[220:223], v[188:191], v[48:63]
	ds_read_b128 v[188:191], v193 offset:56320
	s_mov_b32 m0, s55
	s_add_u32 s44, s34, 0x9000
	s_addc_u32 s45, s35, 0
	global_load_lds_dwordx4 v192, s[44:45] sc1
	v_mfma_f32_32x32x16_f16 v[32:47], a[224:227], v[160:163], v[32:47]
	ds_read_b128 v[160:163], v193 offset:57344
	v_mfma_f32_32x32x16_f16 v[48:63], a[224:227], v[164:167], v[48:63]
	ds_read_b128 v[164:167], v193 offset:58368
	s_waitcnt lgkmcnt(2)
	v_mfma_f32_32x32x16_f16 v[32:47], a[228:231], v[168:171], v[32:47]
	ds_read_b128 v[168:171], v193 offset:59392
	v_mfma_f32_32x32x16_f16 v[48:63], a[228:231], v[172:175], v[48:63]
	ds_read_b128 v[172:175], v193 offset:60416
	global_load_lds_dwordx4 v192, s[44:45] offset:1024 sc1
	v_mfma_f32_32x32x16_f16 v[32:47], a[232:235], v[176:179], v[32:47]
	ds_read_b128 v[176:179], v193 offset:61440
	v_mfma_f32_32x32x16_f16 v[48:63], a[232:235], v[180:183], v[48:63]
	ds_read_b128 v[180:183], v193 offset:62464
	v_mfma_f32_32x32x16_f16 v[32:47], a[236:239], v[184:187], v[32:47]
	ds_read_b128 v[184:187], v193 offset:63488
	v_add_f32_e32 v200, v200, v202
	v_add_f32_e32 v201, v201, v203
	v_add_f32_e32 v200, v200, v204
	v_add_f32_e32 v201, v201, v205
	v_add_f32_e32 v200, v200, v206
	v_add_f32_e32 v201, v201, v207
	global_store_dwordx2 v250, v[200:201], s[72:73]
	v_mfma_f32_32x32x16_f16 v[48:63], a[236:239], v[188:191], v[48:63]
	ds_read_b128 v[188:191], v193 offset:64512
	global_load_lds_dwordx4 v192, s[44:45] offset:2048 sc1
	s_waitcnt vmcnt(9)
	s_barrier
	s_waitcnt lgkmcnt(2)
	v_mfma_f32_32x32x16_f16 v[32:47], a[240:243], v[160:163], v[32:47]
	ds_read_b128 v[160:163], v192 offset:0
	v_mfma_f32_32x32x16_f16 v[48:63], a[240:243], v[164:167], v[48:63]
	ds_read_b128 v[164:167], v192 offset:1024
	v_mfma_f32_32x32x16_f16 v[32:47], a[244:247], v[168:171], v[32:47]
	ds_read_b128 v[168:171], v192 offset:2048
	s_and_b32 s64, s33, 1
	s_lshl_b32 s64, s64, 22
	s_add_u32 s64, s64, s50
	s_add_u32 s64, s64, 0x20000
	s_add_u32 s36, s6, s64
	s_addc_u32 s37, s7, 0
	s_lshl_b32 s64, s33, 3
	s_add_u32 s64, s64, s29
	s_lshl_b32 s64, s64, 5
	s_add_u32 s64, s64, s30
	s_lshl_b32 s64, s64, 2
	s_add_u32 s40, s8, s64
	s_addc_u32 s41, s9, 0
	s_lshl_b32 s64, s33, 19
	s_add_u32 s64, s64, 0x200
	s_add_u32 s72, s62, s64
	s_addc_u32 s73, s63, 0
	v_mfma_f32_32x32x16_f16 v[48:63], a[244:247], v[172:175], v[48:63]
	ds_read_b128 v[172:175], v192 offset:3072
	global_load_lds_dwordx4 v192, s[44:45] offset:3072 sc1
	v_mfma_f32_32x32x16_f16 v[32:47], a[248:251], v[176:179], v[32:47]
	ds_read_b128 v[176:179], v192 offset:4096
	v_mfma_f32_32x32x16_f16 v[48:63], a[248:251], v[180:183], v[48:63]
	ds_read_b128 v[180:183], v192 offset:5120
	s_waitcnt lgkmcnt(2)
	v_mfma_f32_32x32x16_f16 v[32:47], a[252:255], v[184:187], v[32:47]
	ds_read_b128 v[184:187], v192 offset:6144
	v_mfma_f32_32x32x16_f16 v[48:63], a[252:255], v[188:191], v[48:63]
	ds_read_b128 v[188:191], v192 offset:7168
	s_mov_b32 m0, s56
	s_add_u32 s44, s34, 0x10000
	s_addc_u32 s45, s35, 0
	global_load_lds_dwordx4 v192, s[44:45] sc1
	s_nop 3
	s_waitcnt lgkmcnt(2)
	v_mfma_f32_32x32x16_f16 v[64:79], a[0:3], v[160:163], v[64:79]
	ds_read_b128 v[160:163], v192 offset:8192
	v_exp_f32_e32 v200, v32
	v_mfma_f32_32x32x16_f16 v[80:95], a[0:3], v[164:167], v[80:95]
	ds_read_b128 v[164:167], v192 offset:9216
	s_lshl_b32 s64, s71, 3
	s_add_u32 s64, s64, s29
	s_lshl_b32 s64, s64, 7
	s_add_u32 s38, s8, s64
	s_addc_u32 s39, s9, 0
	global_load_dword v251, v196, s[38:39] sc1
	v_exp_f32_e32 v201, v33
	v_add_f32_e32 v200, 1.0, v200
	v_mfma_f32_32x32x16_f16 v[64:79], a[4:7], v[168:171], v[64:79]
	ds_read_b128 v[168:171], v192 offset:10240
	v_exp_f32_e32 v202, v34
	v_add_f32_e32 v201, 1.0, v201
	v_mfma_f32_32x32x16_f16 v[80:95], a[4:7], v[172:175], v[80:95]
	ds_read_b128 v[172:175], v192 offset:11264
	global_load_lds_dwordx4 v192, s[44:45] offset:1024 sc1
	v_exp_f32_e32 v203, v35
	v_add_f32_e32 v202, 1.0, v202
	v_mfma_f32_32x32x16_f16 v[64:79], a[8:11], v[176:179], v[64:79]
	ds_read_b128 v[176:179], v192 offset:12288
	v_exp_f32_e32 v204, v36
	v_add_f32_e32 v203, 1.0, v203
	v_mfma_f32_32x32x16_f16 v[80:95], a[8:11], v[180:183], v[80:95]
	ds_read_b128 v[180:183], v192 offset:13312
	v_exp_f32_e32 v205, v37
	v_add_f32_e32 v204, 1.0, v204
	s_waitcnt lgkmcnt(2)
	v_mfma_f32_32x32x16_f16 v[64:79], a[12:15], v[184:187], v[64:79]
	ds_read_b128 v[184:187], v192 offset:14336
	v_exp_f32_e32 v206, v38
	v_add_f32_e32 v205, 1.0, v205
	v_mfma_f32_32x32x16_f16 v[80:95], a[12:15], v[188:191], v[80:95]
	ds_read_b128 v[188:191], v192 offset:15360
	global_load_lds_dwordx4 v192, s[44:45] offset:2048 sc1
	v_exp_f32_e32 v207, v39
	v_add_f32_e32 v206, 1.0, v206
	v_mfma_f32_32x32x16_f16 v[64:79], a[16:19], v[160:163], v[64:79]
	ds_read_b128 v[160:163], v192 offset:16384
	v_exp_f32_e32 v208, v40
	v_add_f32_e32 v207, 1.0, v207
	v_mfma_f32_32x32x16_f16 v[80:95], a[16:19], v[164:167], v[80:95]
	ds_read_b128 v[164:167], v192 offset:17408
	v_exp_f32_e32 v209, v41
	v_add_f32_e32 v208, 1.0, v208
	v_mfma_f32_32x32x16_f16 v[64:79], a[20:23], v[168:171], v[64:79]
	ds_read_b128 v[168:171], v192 offset:18432
	v_exp_f32_e32 v210, v42
	v_add_f32_e32 v209, 1.0, v209
	v_mfma_f32_32x32x16_f16 v[80:95], a[20:23], v[172:175], v[80:95]
	ds_read_b128 v[172:175], v192 offset:19456
	global_load_lds_dwordx4 v192, s[44:45] offset:3072 sc1
	v_exp_f32_e32 v211, v43
	v_add_f32_e32 v210, 1.0, v210
	s_waitcnt lgkmcnt(2)
	v_mfma_f32_32x32x16_f16 v[64:79], a[24:27], v[176:179], v[64:79]
	ds_read_b128 v[176:179], v192 offset:20480
	v_exp_f32_e32 v212, v44
	v_add_f32_e32 v211, 1.0, v211
	v_mfma_f32_32x32x16_f16 v[80:95], a[24:27], v[180:183], v[80:95]
	ds_read_b128 v[180:183], v192 offset:21504
	v_exp_f32_e32 v213, v45
	v_add_f32_e32 v212, 1.0, v212
	v_mfma_f32_32x32x16_f16 v[64:79], a[28:31], v[184:187], v[64:79]
	ds_read_b128 v[184:187], v192 offset:22528
	v_exp_f32_e32 v214, v46
	v_add_f32_e32 v213, 1.0, v213
	v_mfma_f32_32x32x16_f16 v[80:95], a[28:31], v[188:191], v[80:95]
	ds_read_b128 v[188:191], v192 offset:23552
	s_mov_b32 m0, s57
	s_add_u32 s44, s34, 0x11000
	s_addc_u32 s45, s35, 0
	global_load_lds_dwordx4 v192, s[44:45] sc1
	v_exp_f32_e32 v215, v47
	v_add_f32_e32 v214, 1.0, v214
	v_mfma_f32_32x32x16_f16 v[64:79], a[32:35], v[160:163], v[64:79]
	ds_read_b128 v[160:163], v192 offset:24576
	v_add_f32_e32 v215, 1.0, v215
	v_rcp_f32_e32 v200, v200
	v_mfma_f32_32x32x16_f16 v[80:95], a[32:35], v[164:167], v[80:95]
	ds_read_b128 v[164:167], v192 offset:25600
	v_rcp_f32_e32 v201, v201
	s_waitcnt lgkmcnt(2)
	v_mfma_f32_32x32x16_f16 v[64:79], a[36:39], v[168:171], v[64:79]
	ds_read_b128 v[168:171], v192 offset:26624
	v_rcp_f32_e32 v202, v202
	v_mfma_f32_32x32x16_f16 v[80:95], a[36:39], v[172:175], v[80:95]
	ds_read_b128 v[172:175], v192 offset:27648
	global_load_lds_dwordx4 v192, s[44:45] offset:1024 sc1
	v_rcp_f32_e32 v203, v203
	v_mfma_f32_32x32x16_f16 v[64:79], a[40:43], v[176:179], v[64:79]
	ds_read_b128 v[176:179], v192 offset:28672
	v_rcp_f32_e32 v204, v204
	v_mfma_f32_32x32x16_f16 v[80:95], a[40:43], v[180:183], v[80:95]
	ds_read_b128 v[180:183], v192 offset:29696
	v_rcp_f32_e32 v205, v205
	v_mul_f32_e32 v204, v204, v136
	v_mfma_f32_32x32x16_f16 v[64:79], a[44:47], v[184:187], v[64:79]
	ds_read_b128 v[184:187], v192 offset:30720
	v_rcp_f32_e32 v206, v206
	v_mul_f32_e32 v205, v205, v137
	v_mfma_f32_32x32x16_f16 v[80:95], a[44:47], v[188:191], v[80:95]
	ds_read_b128 v[188:191], v192 offset:31744
	global_load_lds_dwordx4 v192, s[44:45] offset:2048 sc1
	v_rcp_f32_e32 v207, v207
	v_mul_f32_e32 v206, v206, v138
	s_waitcnt vmcnt(8)
	s_barrier
	s_waitcnt lgkmcnt(2)
	v_mfma_f32_32x32x16_f16 v[64:79], a[48:51], v[160:163], v[64:79]
	ds_read_b128 v[160:163], v192 offset:32768
	v_rcp_f32_e32 v208, v208
	v_mul_f32_e32 v207, v207, v139
	v_mfma_f32_32x32x16_f16 v[80:95], a[48:51], v[164:167], v[80:95]
	ds_read_b128 v[164:167], v192 offset:33792
	v_rcp_f32_e32 v209, v209
	v_fmamk_f32 v208, v208, 0xc0b8aa3b, v198
	v_mfma_f32_32x32x16_f16 v[64:79], a[52:55], v[168:171], v[64:79]
	ds_read_b128 v[168:171], v192 offset:34816
	v_rcp_f32_e32 v210, v210
	v_fmamk_f32 v209, v209, 0xc0b8aa3b, v198
	v_fma_f32 v136, v200, v208, v204
	v_mfma_f32_32x32x16_f16 v[80:95], a[52:55], v[172:175], v[80:95]
	ds_read_b128 v[172:175], v192 offset:35840
	global_load_lds_dwordx4 v192, s[44:45] offset:3072 sc1
	v_rcp_f32_e32 v211, v211
	v_fmamk_f32 v210, v210, 0xc0b8aa3b, v198
	v_fma_f32 v137, v201, v209, v205
	v_mfma_f32_32x32x16_f16 v[64:79], a[56:59], v[176:179], v[64:79]
	ds_read_b128 v[176:179], v192 offset:36864
	v_rcp_f32_e32 v212, v212
	v_fmamk_f32 v211, v211, 0xc0b8aa3b, v198
	v_fma_f32 v138, v202, v210, v206
	v_mfma_f32_32x32x16_f16 v[80:95], a[56:59], v[180:183], v[80:95]
	ds_read_b128 v[180:183], v192 offset:37888
	v_rcp_f32_e32 v213, v213
	v_fma_f32 v139, v203, v211, v207
	s_waitcnt lgkmcnt(2)
	v_mfma_f32_32x32x16_f16 v[64:79], a[60:63], v[184:187], v[64:79]
	ds_read_b128 v[184:187], v192 offset:38912
	v_rcp_f32_e32 v214, v214
	v_mfma_f32_32x32x16_f16 v[80:95], a[60:63], v[188:191], v[80:95]
	ds_read_b128 v[188:191], v192 offset:39936
	s_mov_b32 m0, s58
	s_add_u32 s44, s34, 0x18000
	s_addc_u32 s45, s35, 0
	global_load_lds_dwordx4 v192, s[44:45] sc1
	v_rcp_f32_e32 v215, v215
	v_mfma_f32_32x32x16_f16 v[64:79], a[64:67], v[160:163], v[64:79]
	ds_read_b128 v[160:163], v192 offset:40960
	v_exp_f32_e32 v200, v136
	v_mfma_f32_32x32x16_f16 v[80:95], a[64:67], v[164:167], v[80:95]
	ds_read_b128 v[164:167], v192 offset:41984
	v_exp_f32_e32 v201, v137
	v_add_f32_e32 v200, 1.0, v200
	v_mfma_f32_32x32x16_f16 v[64:79], a[68:71], v[168:171], v[64:79]
	ds_read_b128 v[168:171], v192 offset:43008
	v_exp_f32_e32 v202, v138
	v_add_f32_e32 v201, 1.0, v201
	v_mfma_f32_32x32x16_f16 v[80:95], a[68:71], v[172:175], v[80:95]
	ds_read_b128 v[172:175], v192 offset:44032
	global_load_lds_dwordx4 v192, s[44:45] offset:1024 sc1
	v_exp_f32_e32 v203, v139
	v_add_f32_e32 v202, 1.0, v202
	s_waitcnt lgkmcnt(2)
	v_mfma_f32_32x32x16_f16 v[64:79], a[72:75], v[176:179], v[64:79]
	ds_read_b128 v[176:179], v192 offset:45056
	v_add_f32_e32 v203, 1.0, v203
	v_rcp_f32_e32 v200, v200
	v_mfma_f32_32x32x16_f16 v[80:95], a[72:75], v[180:183], v[80:95]
	ds_read_b128 v[180:183], v192 offset:46080
	v_rcp_f32_e32 v201, v201
	v_fma_f32 v200, v200, 2.0, -1.0
	v_mfma_f32_32x32x16_f16 v[64:79], a[76:79], v[184:187], v[64:79]
	ds_read_b128 v[184:187], v192 offset:47104
	v_rcp_f32_e32 v202, v202
	v_fma_f32 v201, v201, 2.0, -1.0
	v_mul_f32_e32 v216, v212, v200
	v_mfma_f32_32x32x16_f16 v[80:95], a[76:79], v[188:191], v[80:95]
	ds_read_b128 v[188:191], v192 offset:48128
	global_load_lds_dwordx4 v192, s[44:45] offset:2048 sc1
	v_rcp_f32_e32 v203, v203
	v_fma_f32 v202, v202, 2.0, -1.0
	v_mul_f32_e32 v217, v213, v201
	v_mfma_f32_32x32x16_f16 v[64:79], a[80:83], v[160:163], v[64:79]
	ds_read_b128 v[160:163], v192 offset:49152
	v_fma_f32 v203, v203, 2.0, -1.0
	v_mul_f32_e32 v218, v214, v202
	v_exp_f32_e32 v200, v48
	v_mfma_f32_32x32x16_f16 v[80:95], a[80:83], v[164:167], v[80:95]
	ds_read_b128 v[164:167], v192 offset:50176
	v_mul_f32_e32 v219, v215, v203
	v_mul_f32_e32 v236, v216, v228
	v_exp_f32_e32 v201, v49
	s_waitcnt lgkmcnt(2)
	v_mfma_f32_32x32x16_f16 v[64:79], a[84:87], v[168:171], v[64:79]
	ds_read_b128 v[168:171], v192 offset:51200
	v_mul_f32_e32 v237, v216, v232
	v_fmac_f32_e32 v236, v217, v229
	v_exp_f32_e32 v202, v50
	v_mfma_f32_32x32x16_f16 v[80:95], a[84:87], v[172:175], v[80:95]
	ds_read_b128 v[172:175], v192 offset:52224
	global_load_lds_dwordx4 v192, s[44:45] offset:3072 sc1
	v_fmac_f32_e32 v237, v217, v233
	v_fmac_f32_e32 v236, v218, v230
	v_exp_f32_e32 v203, v51
	v_mfma_f32_32x32x16_f16 v[64:79], a[88:91], v[176:179], v[64:79]
	ds_read_b128 v[176:179], v192 offset:53248
	v_fmac_f32_e32 v237, v218, v234
	v_fmac_f32_e32 v236, v219, v231
	v_exp_f32_e32 v204, v52
	v_mfma_f32_32x32x16_f16 v[80:95], a[88:91], v[180:183], v[80:95]
	ds_read_b128 v[180:183], v192 offset:54272
	v_fmac_f32_e32 v237, v219, v235
	v_mov_b32_e32 v238, v236
	v_exp_f32_e32 v205, v53
	v_mfma_f32_32x32x16_f16 v[64:79], a[92:95], v[184:187], v[64:79]
	ds_read_b128 v[184:187], v192 offset:55296
	v_mov_b32_e32 v240, v237
	v_cvt_pk_f16_f32 v220, v216, v217
	v_exp_f32_e32 v206, v54
	v_mfma_f32_32x32x16_f16 v[80:95], a[92:95], v[188:191], v[80:95]
	ds_read_b128 v[188:191], v192 offset:56320
	s_mov_b32 m0, s59
	s_add_u32 s44, s34, 0x19000
	s_addc_u32 s45, s35, 0
	global_load_lds_dwordx4 v192, s[44:45] sc1
	v_permlane32_swap_b32_e32 v236, v238
	v_permlane32_swap_b32_e32 v237, v240
	v_add_f32_e32 v238, v236, v238
	v_add_f32_e32 v239, v237, v240
	ds_write_b64 v248, v[238:239] offset:512
	v_exp_f32_e32 v207, v55
	s_waitcnt lgkmcnt(3)
	v_mfma_f32_32x32x16_f16 v[64:79], a[96:99], v[160:163], v[64:79]
	ds_read_b128 v[160:163], v192 offset:57344
	v_cvt_pk_f16_f32 v221, v218, v219
	v_exp_f32_e32 v208, v56
	v_add_f32_e32 v200, 1.0, v200
	v_mfma_f32_32x32x16_f16 v[80:95], a[96:99], v[164:167], v[80:95]
	ds_read_b128 v[164:167], v192 offset:58368
	v_exp_f32_e32 v209, v57
	v_add_f32_e32 v201, 1.0, v201
	v_add_f32_e32 v202, 1.0, v202
	v_mfma_f32_32x32x16_f16 v[64:79], a[100:103], v[168:171], v[64:79]
	ds_read_b128 v[168:171], v192 offset:59392
	v_exp_f32_e32 v210, v58
	v_add_f32_e32 v203, 1.0, v203
	v_add_f32_e32 v204, 1.0, v204
	v_mfma_f32_32x32x16_f16 v[80:95], a[100:103], v[172:175], v[80:95]
	ds_read_b128 v[172:175], v192 offset:60416
	global_load_lds_dwordx4 v192, s[44:45] offset:1024 sc1
	v_exp_f32_e32 v211, v59
	v_add_f32_e32 v205, 1.0, v205
	v_add_f32_e32 v206, 1.0, v206
	v_mfma_f32_32x32x16_f16 v[64:79], a[104:107], v[176:179], v[64:79]
	ds_read_b128 v[176:179], v192 offset:61440
	v_exp_f32_e32 v212, v60
	v_add_f32_e32 v207, 1.0, v207
	v_add_f32_e32 v208, 1.0, v208
	v_mfma_f32_32x32x16_f16 v[80:95], a[104:107], v[180:183], v[80:95]
	ds_read_b128 v[180:183], v192 offset:62464
	v_exp_f32_e32 v213, v61
	v_add_f32_e32 v209, 1.0, v209
	v_add_f32_e32 v210, 1.0, v210
	s_waitcnt lgkmcnt(2)
	v_mfma_f32_32x32x16_f16 v[64:79], a[108:111], v[184:187], v[64:79]
	ds_read_b128 v[184:187], v192 offset:63488
	v_exp_f32_e32 v214, v62
	v_add_f32_e32 v211, 1.0, v211
	v_add_f32_e32 v212, 1.0, v212
	v_mfma_f32_32x32x16_f16 v[80:95], a[108:111], v[188:191], v[80:95]
	ds_read_b128 v[188:191], v192 offset:64512
	global_load_lds_dwordx4 v192, s[44:45] offset:2048 sc1
	v_exp_f32_e32 v215, v63
	v_add_f32_e32 v213, 1.0, v213
	v_add_f32_e32 v214, 1.0, v214
	s_waitcnt vmcnt(7)
	s_barrier
	v_mfma_f32_32x32x16_f16 v[64:79], a[112:115], v[160:163], v[64:79]
	ds_read_b128 v[160:163], v193 offset:0
	v_add_f32_e32 v215, 1.0, v215
	v_rcp_f32_e32 v200, v200
	v_mfma_f32_32x32x16_f16 v[80:95], a[112:115], v[164:167], v[80:95]
	ds_read_b128 v[164:167], v193 offset:1024
	v_rcp_f32_e32 v201, v201
	v_mfma_f32_32x32x16_f16 v[64:79], a[116:119], v[168:171], v[64:79]
	ds_read_b128 v[168:171], v193 offset:2048
	v_rcp_f32_e32 v202, v202
	v_mfma_f32_32x32x16_f16 v[80:95], a[116:119], v[172:175], v[80:95]
	ds_read_b128 v[172:175], v193 offset:3072
	global_load_lds_dwordx4 v192, s[44:45] offset:3072 sc1
	v_rcp_f32_e32 v203, v203
	s_waitcnt lgkmcnt(2)
	v_mfma_f32_32x32x16_f16 v[64:79], a[120:123], v[176:179], v[64:79]
	ds_read_b128 v[176:179], v193 offset:4096
	v_rcp_f32_e32 v204, v204
	v_mfma_f32_32x32x16_f16 v[80:95], a[120:123], v[180:183], v[80:95]
	ds_read_b128 v[180:183], v193 offset:5120
	v_rcp_f32_e32 v205, v205
	v_mul_f32_e32 v204, v204, v140
	v_mfma_f32_32x32x16_f16 v[64:79], a[124:127], v[184:187], v[64:79]
	ds_read_b128 v[184:187], v193 offset:6144
	v_rcp_f32_e32 v206, v206
	v_mul_f32_e32 v205, v205, v141
	v_mfma_f32_32x32x16_f16 v[80:95], a[124:127], v[188:191], v[80:95]
	ds_read_b128 v[188:191], v193 offset:7168
	v_cmp_gt_u32_e32 vcc, 4, v251
	s_cbranch_vccnz .LD_tpoll29
.LD_tok28:
	s_and_b32 s64, s71, 1
	s_lshl_b32 s64, s64, 22
	s_add_u32 s64, s64, s49
	s_add_u32 s64, s64, 0x60000
	s_add_u32 s34, s6, s64
	s_addc_u32 s35, s7, 0
	s_mov_b32 m0, s52
	s_add_u32 s44, s34, 0x0
	s_addc_u32 s45, s35, 0
	global_load_lds_dwordx4 v192, s[44:45] sc1
	v_rcp_f32_e32 v207, v207
	v_mul_f32_e32 v206, v206, v142
	v_mfma_f32_32x32x16_f16 v[64:79], a[128:131], v[160:163], v[64:79]
	ds_read_b128 v[160:163], v193 offset:8192
	v_rcp_f32_e32 v208, v208
	v_mul_f32_e32 v207, v207, v143
	v_mfma_f32_32x32x16_f16 v[80:95], a[128:131], v[164:167], v[80:95]
	ds_read_b128 v[164:167], v193 offset:9216
	v_rcp_f32_e32 v209, v209
	v_fmamk_f32 v208, v208, 0xc0b8aa3b, v198
	s_waitcnt lgkmcnt(2)
	v_mfma_f32_32x32x16_f16 v[64:79], a[132:135], v[168:171], v[64:79]
	ds_read_b128 v[168:171], v193 offset:10240
	v_rcp_f32_e32 v210, v210
	v_fmamk_f32 v209, v209, 0xc0b8aa3b, v198
	v_fma_f32 v140, v200, v208, v204
	s_add_u32 s46, s42, 0x0
	s_addc_u32 s47, s43, 0
	global_load_dwordx4 v[0:3], v192, s[46:47] offset:0
	v_mfma_f32_32x32x16_f16 v[80:95], a[132:135], v[172:175], v[80:95]
	ds_read_b128 v[172:175], v193 offset:11264
	global_load_lds_dwordx4 v192, s[44:45] offset:1024 sc1
	v_rcp_f32_e32 v211, v211
	v_fmamk_f32 v210, v210, 0xc0b8aa3b, v198
	v_fma_f32 v141, v201, v209, v205
	global_load_dwordx4 v[4:7], v192, s[46:47] offset:1024
	global_load_dwordx4 v[8:11], v192, s[46:47] offset:2048
	v_mfma_f32_32x32x16_f16 v[64:79], a[136:139], v[176:179], v[64:79]
	ds_read_b128 v[176:179], v193 offset:12288
	v_rcp_f32_e32 v212, v212
	v_fmamk_f32 v211, v211, 0xc0b8aa3b, v198
	v_fma_f32 v142, v202, v210, v206
	global_load_dwordx4 v[12:15], v192, s[46:47] offset:3072
	s_add_u32 s46, s42, 0x1000
	s_addc_u32 s47, s43, 0
	v_mfma_f32_32x32x16_f16 v[80:95], a[136:139], v[180:183], v[80:95]
	ds_read_b128 v[180:183], v193 offset:13312
	v_rcp_f32_e32 v213, v213
	v_fma_f32 v143, v203, v211, v207
	global_load_dwordx4 v[16:19], v192, s[46:47] offset:0
	global_load_dwordx4 v[20:23], v192, s[46:47] offset:1024
	v_mfma_f32_32x32x16_f16 v[64:79], a[140:143], v[184:187], v[64:79]
	ds_read_b128 v[184:187], v193 offset:14336
	v_rcp_f32_e32 v214, v214
	global_load_dwordx4 v[24:27], v192, s[46:47] offset:2048
	global_load_dwordx4 v[28:31], v192, s[46:47] offset:3072
	v_mfma_f32_32x32x16_f16 v[80:95], a[140:143], v[188:191], v[80:95]
	ds_read_b128 v[188:191], v193 offset:15360
	global_load_lds_dwordx4 v192, s[44:45] offset:2048 sc1
	v_rcp_f32_e32 v215, v215
	s_waitcnt lgkmcnt(2)
	v_mfma_f32_32x32x16_f16 v[64:79], a[144:147], v[160:163], v[64:79]
	ds_read_b128 v[160:163], v193 offset:16384
	v_exp_f32_e32 v200, v140
	v_mfma_f32_32x32x16_f16 v[80:95], a[144:147], v[164:167], v[80:95]
	ds_read_b128 v[164:167], v193 offset:17408
	v_exp_f32_e32 v201, v141
	v_add_f32_e32 v200, 1.0, v200
	v_mfma_f32_32x32x16_f16 v[64:79], a[148:151], v[168:171], v[64:79]
	ds_read_b128 v[168:171], v193 offset:18432
	v_exp_f32_e32 v202, v142
	v_add_f32_e32 v201, 1.0, v201
	v_mfma_f32_32x32x16_f16 v[80:95], a[148:151], v[172:175], v[80:95]
	ds_read_b128 v[172:175], v193 offset:19456
	global_load_lds_dwordx4 v192, s[44:45] offset:3072 sc1
	v_exp_f32_e32 v203, v143
	v_add_f32_e32 v202, 1.0, v202
	v_mfma_f32_32x32x16_f16 v[64:79], a[152:155], v[176:179], v[64:79]
	ds_read_b128 v[176:179], v193 offset:20480
	v_add_f32_e32 v203, 1.0, v203
	v_rcp_f32_e32 v200, v200
	v_mfma_f32_32x32x16_f16 v[80:95], a[152:155], v[180:183], v[80:95]
	ds_read_b128 v[180:183], v193 offset:21504
	v_rcp_f32_e32 v201, v201
	v_fma_f32 v200, v200, 2.0, -1.0
	s_waitcnt lgkmcnt(2)
	v_mfma_f32_32x32x16_f16 v[64:79], a[156:159], v[184:187], v[64:79]
	ds_read_b128 v[184:187], v193 offset:22528
	v_rcp_f32_e32 v202, v202
	v_fma_f32 v201, v201, 2.0, -1.0
	v_mul_f32_e32 v216, v212, v200
	v_mfma_f32_32x32x16_f16 v[80:95], a[156:159], v[188:191], v[80:95]
	ds_read_b128 v[188:191], v193 offset:23552
	s_mov_b32 m0, s53
	s_add_u32 s44, s34, 0x1000
	s_addc_u32 s45, s35, 0
	global_load_lds_dwordx4 v192, s[44:45] sc1
	v_rcp_f32_e32 v203, v203
	v_fma_f32 v202, v202, 2.0, -1.0
	v_mul_f32_e32 v217, v213, v201
	v_mfma_f32_32x32x16_f16 v[64:79], a[160:163], v[160:163], v[64:79]
	ds_read_b128 v[160:163], v193 offset:24576
	v_fma_f32 v203, v203, 2.0, -1.0
	v_mul_f32_e32 v218, v214, v202
	v_mfma_f32_32x32x16_f16 v[80:95], a[160:163], v[164:167], v[80:95]
	ds_read_b128 v[164:167], v193 offset:25600
	v_mul_f32_e32 v219, v215, v203
	v_mul_f32_e32 v236, v216, v228
	v_mfma_f32_32x32x16_f16 v[64:79], a[164:167], v[168:171], v[64:79]
	ds_read_b128 v[168:171], v193 offset:26624
	v_mul_f32_e32 v237, v216, v232
	v_fmac_f32_e32 v236, v217, v229
	v_mfma_f32_32x32x16_f16 v[80:95], a[164:167], v[172:175], v[80:95]
	ds_read_b128 v[172:175], v193 offset:27648
	global_load_lds_dwordx4 v192, s[44:45] offset:1024 sc1
	v_fmac_f32_e32 v237, v217, v233
	v_fmac_f32_e32 v236, v218, v230
	s_waitcnt lgkmcnt(2)
	v_mfma_f32_32x32x16_f16 v[64:79], a[168:171], v[176:179], v[64:79]
	ds_read_b128 v[176:179], v193 offset:28672
	v_fmac_f32_e32 v237, v218, v234
	v_fmac_f32_e32 v236, v219, v231
	v_mfma_f32_32x32x16_f16 v[80:95], a[168:171], v[180:183], v[80:95]
	ds_read_b128 v[180:183], v193 offset:29696
	v_fmac_f32_e32 v237, v219, v235
	v_mov_b32_e32 v238, v236
	v_mfma_f32_32x32x16_f16 v[64:79], a[172:175], v[184:187], v[64:79]
	ds_read_b128 v[184:187], v193 offset:30720
	v_mov_b32_e32 v240, v237
	v_cvt_pk_f16_f32 v222, v216, v217
	v_mfma_f32_32x32x16_f16 v[80:95], a[172:175], v[188:191], v[80:95]
	ds_read_b128 v[188:191], v193 offset:31744
	global_load_lds_dwordx4 v192, s[44:45] offset:2048 sc1
	v_permlane32_swap_b32_e32 v236, v238
	v_permlane32_swap_b32_e32 v237, v240
	v_add_f32_e32 v238, v236, v238
	v_add_f32_e32 v239, v237, v240
	ds_write_b64 v248, v[238:239] offset:768
	s_waitcnt vmcnt(15)
	s_barrier
	v_mfma_f32_32x32x16_f16 v[64:79], a[176:179], v[160:163], v[64:79]
	ds_read_b128 v[160:163], v193 offset:32768
	v_cvt_pk_f16_f32 v223, v218, v219
	v_mfma_f32_32x32x16_f16 v[80:95], a[176:179], v[164:167], v[80:95]
	ds_read_b128 v[164:167], v193 offset:33792
	v_permlane32_swap_b32_e32 v220, v222
	v_permlane32_swap_b32_e32 v221, v223
	s_cmp_eq_u32 s31, 0
	s_cbranch_scc1 .LD_slow30
	global_store_dwordx4 v195, v[220:223], s[36:37] offset:0

.LD_join33:
	ds_read_b64 v[200:201], v249 offset:512
	ds_read_b64 v[202:203], v249 offset:2560
	ds_read_b64 v[204:205], v249 offset:4608
	ds_read_b64 v[206:207], v249 offset:6656
	v_mfma_f32_32x32x16_f16 v[80:95], a[212:215], v[172:175], v[80:95]
	ds_read_b128 v[172:175], v193 offset:52224
	global_load_lds_dwordx4 v192, s[44:45] offset:3072 sc1
	s_waitcnt lgkmcnt(6)
	v_mfma_f32_32x32x16_f16 v[64:79], a[216:219], v[176:179], v[64:79]
	ds_read_b128 v[176:179], v193 offset:53248
	v_mfma_f32_32x32x16_f16 v[80:95], a[216:219], v[180:183], v[80:95]
	ds_read_b128 v[180:183], v193 offset:54272
	v_mfma_f32_32x32x16_f16 v[64:79], a[220:223], v[184:187], v[64:79]
	ds_read_b128 v[184:187], v193 offset:55296
	v_mfma_f32_32x32x16_f16 v[80:95], a[220:223], v[188:191], v[80:95]
	ds_read_b128 v[188:191], v193 offset:56320
	s_mov_b32 m0, s55
	s_add_u32 s44, s34, 0x9000
	s_addc_u32 s45, s35, 0
	global_load_lds_dwordx4 v192, s[44:45] sc1
	v_mfma_f32_32x32x16_f16 v[64:79], a[224:227], v[160:163], v[64:79]
	ds_read_b128 v[160:163], v193 offset:57344
	v_mfma_f32_32x32x16_f16 v[80:95], a[224:227], v[164:167], v[80:95]
	ds_read_b128 v[164:167], v193 offset:58368
	s_waitcnt lgkmcnt(2)
	v_mfma_f32_32x32x16_f16 v[64:79], a[228:231], v[168:171], v[64:79]
	ds_read_b128 v[168:171], v193 offset:59392
	v_mfma_f32_32x32x16_f16 v[80:95], a[228:231], v[172:175], v[80:95]
	ds_read_b128 v[172:175], v193 offset:60416
	global_load_lds_dwordx4 v192, s[44:45] offset:1024 sc1
	v_mfma_f32_32x32x16_f16 v[64:79], a[232:235], v[176:179], v[64:79]
	ds_read_b128 v[176:179], v193 offset:61440
	v_mfma_f32_32x32x16_f16 v[80:95], a[232:235], v[180:183], v[80:95]
	ds_read_b128 v[180:183], v193 offset:62464
	v_mfma_f32_32x32x16_f16 v[64:79], a[236:239], v[184:187], v[64:79]
	ds_read_b128 v[184:187], v193 offset:63488
	v_add_f32_e32 v200, v200, v202
	v_add_f32_e32 v201, v201, v203
	v_add_f32_e32 v200, v200, v204
	v_add_f32_e32 v201, v201, v205
	v_add_f32_e32 v200, v200, v206
	v_add_f32_e32 v201, v201, v207
	global_store_dwordx2 v250, v[200:201], s[72:73]
	v_mfma_f32_32x32x16_f16 v[80:95], a[236:239], v[188:191], v[80:95]
	ds_read_b128 v[188:191], v193 offset:64512
	global_load_lds_dwordx4 v192, s[44:45] offset:2048 sc1
	s_waitcnt vmcnt(9)
	s_barrier
	s_waitcnt lgkmcnt(2)
	v_mfma_f32_32x32x16_f16 v[64:79], a[240:243], v[160:163], v[64:79]
	ds_read_b128 v[160:163], v192 offset:0
	v_mfma_f32_32x32x16_f16 v[80:95], a[240:243], v[164:167], v[80:95]
	ds_read_b128 v[164:167], v192 offset:1024
	v_mfma_f32_32x32x16_f16 v[64:79], a[244:247], v[168:171], v[64:79]
	ds_read_b128 v[168:171], v192 offset:2048
	s_and_b32 s64, s33, 1
	s_lshl_b32 s64, s64, 22
	s_add_u32 s64, s64, s50
	s_add_u32 s64, s64, 0x40000
	s_add_u32 s36, s6, s64
	s_addc_u32 s37, s7, 0
	s_lshl_b32 s64, s33, 3
	s_add_u32 s64, s64, s29
	s_lshl_b32 s64, s64, 5
	s_add_u32 s64, s64, s30
	s_lshl_b32 s64, s64, 2
	s_add_u32 s40, s8, s64
	s_addc_u32 s41, s9, 0
	s_lshl_b32 s64, s33, 19
	s_add_u32 s64, s64, 0x400
	s_add_u32 s72, s62, s64
	s_addc_u32 s73, s63, 0
	v_mfma_f32_32x32x16_f16 v[80:95], a[244:247], v[172:175], v[80:95]
	ds_read_b128 v[172:175], v192 offset:3072
	global_load_lds_dwordx4 v192, s[44:45] offset:3072 sc1
	v_mfma_f32_32x32x16_f16 v[64:79], a[248:251], v[176:179], v[64:79]
	ds_read_b128 v[176:179], v192 offset:4096
	v_mfma_f32_32x32x16_f16 v[80:95], a[248:251], v[180:183], v[80:95]
	ds_read_b128 v[180:183], v192 offset:5120
	s_waitcnt lgkmcnt(2)
	v_mfma_f32_32x32x16_f16 v[64:79], a[252:255], v[184:187], v[64:79]
	ds_read_b128 v[184:187], v192 offset:6144
	v_mfma_f32_32x32x16_f16 v[80:95], a[252:255], v[188:191], v[80:95]
	ds_read_b128 v[188:191], v192 offset:7168
	s_mov_b32 m0, s56
	s_add_u32 s44, s34, 0x10000
	s_addc_u32 s45, s35, 0
	global_load_lds_dwordx4 v192, s[44:45] sc1
	s_nop 3
	s_waitcnt lgkmcnt(2)
	v_mfma_f32_32x32x16_f16 v[96:111], a[0:3], v[160:163], v[96:111]
	ds_read_b128 v[160:163], v192 offset:8192
	v_exp_f32_e32 v200, v64
	v_mfma_f32_32x32x16_f16 v[112:127], a[0:3], v[164:167], v[112:127]
	ds_read_b128 v[164:167], v192 offset:9216
	s_lshl_b32 s64, s33, 3
	s_add_u32 s64, s64, s29
	s_lshl_b32 s64, s64, 7
	s_add_u32 s38, s8, s64
	s_addc_u32 s39, s9, 0
	global_load_dword v251, v196, s[38:39] sc1
	v_exp_f32_e32 v201, v65
	v_add_f32_e32 v200, 1.0, v200
	v_mfma_f32_32x32x16_f16 v[96:111], a[4:7], v[168:171], v[96:111]
	ds_read_b128 v[168:171], v192 offset:10240
	v_exp_f32_e32 v202, v66
	v_add_f32_e32 v201, 1.0, v201
	v_mfma_f32_32x32x16_f16 v[112:127], a[4:7], v[172:175], v[112:127]
	ds_read_b128 v[172:175], v192 offset:11264
	global_load_lds_dwordx4 v192, s[44:45] offset:1024 sc1
	v_exp_f32_e32 v203, v67
	v_add_f32_e32 v202, 1.0, v202
	v_mfma_f32_32x32x16_f16 v[96:111], a[8:11], v[176:179], v[96:111]
	ds_read_b128 v[176:179], v192 offset:12288
	v_exp_f32_e32 v204, v68
	v_add_f32_e32 v203, 1.0, v203
	v_mfma_f32_32x32x16_f16 v[112:127], a[8:11], v[180:183], v[112:127]
	ds_read_b128 v[180:183], v192 offset:13312
	v_exp_f32_e32 v205, v69
	v_add_f32_e32 v204, 1.0, v204
	s_waitcnt lgkmcnt(2)
	v_mfma_f32_32x32x16_f16 v[96:111], a[12:15], v[184:187], v[96:111]
	ds_read_b128 v[184:187], v192 offset:14336
	v_exp_f32_e32 v206, v70
	v_add_f32_e32 v205, 1.0, v205
	v_mfma_f32_32x32x16_f16 v[112:127], a[12:15], v[188:191], v[112:127]
	ds_read_b128 v[188:191], v192 offset:15360
	global_load_lds_dwordx4 v192, s[44:45] offset:2048 sc1
	v_exp_f32_e32 v207, v71
	v_add_f32_e32 v206, 1.0, v206
	v_mfma_f32_32x32x16_f16 v[96:111], a[16:19], v[160:163], v[96:111]
	ds_read_b128 v[160:163], v192 offset:16384
	v_exp_f32_e32 v208, v72
	v_add_f32_e32 v207, 1.0, v207
	v_mfma_f32_32x32x16_f16 v[112:127], a[16:19], v[164:167], v[112:127]
	ds_read_b128 v[164:167], v192 offset:17408
	v_exp_f32_e32 v209, v73
	v_add_f32_e32 v208, 1.0, v208
	v_mfma_f32_32x32x16_f16 v[96:111], a[20:23], v[168:171], v[96:111]
	ds_read_b128 v[168:171], v192 offset:18432
	v_exp_f32_e32 v210, v74
	v_add_f32_e32 v209, 1.0, v209
	v_mfma_f32_32x32x16_f16 v[112:127], a[20:23], v[172:175], v[112:127]
	ds_read_b128 v[172:175], v192 offset:19456
	global_load_lds_dwordx4 v192, s[44:45] offset:3072 sc1
	v_exp_f32_e32 v211, v75
	v_add_f32_e32 v210, 1.0, v210
	s_waitcnt lgkmcnt(2)
	v_mfma_f32_32x32x16_f16 v[96:111], a[24:27], v[176:179], v[96:111]
	ds_read_b128 v[176:179], v192 offset:20480
	v_exp_f32_e32 v212, v76
	v_add_f32_e32 v211, 1.0, v211
	v_mfma_f32_32x32x16_f16 v[112:127], a[24:27], v[180:183], v[112:127]
	ds_read_b128 v[180:183], v192 offset:21504
	v_exp_f32_e32 v213, v77
	v_add_f32_e32 v212, 1.0, v212
	v_mfma_f32_32x32x16_f16 v[96:111], a[28:31], v[184:187], v[96:111]
	ds_read_b128 v[184:187], v192 offset:22528
	v_exp_f32_e32 v214, v78
	v_add_f32_e32 v213, 1.0, v213
	v_mfma_f32_32x32x16_f16 v[112:127], a[28:31], v[188:191], v[112:127]
	ds_read_b128 v[188:191], v192 offset:23552
	s_mov_b32 m0, s57
	s_add_u32 s44, s34, 0x11000
	s_addc_u32 s45, s35, 0
	global_load_lds_dwordx4 v192, s[44:45] sc1
	v_exp_f32_e32 v215, v79
	v_add_f32_e32 v214, 1.0, v214
	v_mfma_f32_32x32x16_f16 v[96:111], a[32:35], v[160:163], v[96:111]
	ds_read_b128 v[160:163], v192 offset:24576
	v_add_f32_e32 v215, 1.0, v215
	v_rcp_f32_e32 v200, v200
	v_mfma_f32_32x32x16_f16 v[112:127], a[32:35], v[164:167], v[112:127]
	ds_read_b128 v[164:167], v192 offset:25600
	v_rcp_f32_e32 v201, v201
	s_waitcnt lgkmcnt(2)
	v_mfma_f32_32x32x16_f16 v[96:111], a[36:39], v[168:171], v[96:111]
	ds_read_b128 v[168:171], v192 offset:26624
	v_rcp_f32_e32 v202, v202
	v_mfma_f32_32x32x16_f16 v[112:127], a[36:39], v[172:175], v[112:127]
	ds_read_b128 v[172:175], v192 offset:27648
	global_load_lds_dwordx4 v192, s[44:45] offset:1024 sc1
	v_rcp_f32_e32 v203, v203
	v_mfma_f32_32x32x16_f16 v[96:111], a[40:43], v[176:179], v[96:111]
	ds_read_b128 v[176:179], v192 offset:28672
	v_rcp_f32_e32 v204, v204
	v_mfma_f32_32x32x16_f16 v[112:127], a[40:43], v[180:183], v[112:127]
	ds_read_b128 v[180:183], v192 offset:29696
	v_rcp_f32_e32 v205, v205
	v_mul_f32_e32 v204, v204, v144
	v_mfma_f32_32x32x16_f16 v[96:111], a[44:47], v[184:187], v[96:111]
	ds_read_b128 v[184:187], v192 offset:30720
	v_rcp_f32_e32 v206, v206
	v_mul_f32_e32 v205, v205, v145
	v_mfma_f32_32x32x16_f16 v[112:127], a[44:47], v[188:191], v[112:127]
	ds_read_b128 v[188:191], v192 offset:31744
	global_load_lds_dwordx4 v192, s[44:45] offset:2048 sc1
	v_rcp_f32_e32 v207, v207
	v_mul_f32_e32 v206, v206, v146
	s_waitcnt vmcnt(8)
	s_barrier
	s_waitcnt lgkmcnt(2)
	v_mfma_f32_32x32x16_f16 v[96:111], a[48:51], v[160:163], v[96:111]
	ds_read_b128 v[160:163], v192 offset:32768
	v_rcp_f32_e32 v208, v208
	v_mul_f32_e32 v207, v207, v147
	v_mfma_f32_32x32x16_f16 v[112:127], a[48:51], v[164:167], v[112:127]
	ds_read_b128 v[164:167], v192 offset:33792
	v_rcp_f32_e32 v209, v209
	v_fmamk_f32 v208, v208, 0xc0b8aa3b, v198
	v_mfma_f32_32x32x16_f16 v[96:111], a[52:55], v[168:171], v[96:111]
	ds_read_b128 v[168:171], v192 offset:34816
	v_rcp_f32_e32 v210, v210
	v_fmamk_f32 v209, v209, 0xc0b8aa3b, v198
	v_fma_f32 v144, v200, v208, v204
	v_mfma_f32_32x32x16_f16 v[112:127], a[52:55], v[172:175], v[112:127]
	ds_read_b128 v[172:175], v192 offset:35840
	global_load_lds_dwordx4 v192, s[44:45] offset:3072 sc1
	v_rcp_f32_e32 v211, v211
	v_fmamk_f32 v210, v210, 0xc0b8aa3b, v198
	v_fma_f32 v145, v201, v209, v205
	v_mfma_f32_32x32x16_f16 v[96:111], a[56:59], v[176:179], v[96:111]
	ds_read_b128 v[176:179], v192 offset:36864
	v_rcp_f32_e32 v212, v212
	v_fmamk_f32 v211, v211, 0xc0b8aa3b, v198
	v_fma_f32 v146, v202, v210, v206
	v_mfma_f32_32x32x16_f16 v[112:127], a[56:59], v[180:183], v[112:127]
	ds_read_b128 v[180:183], v192 offset:37888
	v_rcp_f32_e32 v213, v213
	v_fma_f32 v147, v203, v211, v207
	s_waitcnt lgkmcnt(2)
	v_mfma_f32_32x32x16_f16 v[96:111], a[60:63], v[184:187], v[96:111]
	ds_read_b128 v[184:187], v192 offset:38912
	v_rcp_f32_e32 v214, v214
	v_mfma_f32_32x32x16_f16 v[112:127], a[60:63], v[188:191], v[112:127]
	ds_read_b128 v[188:191], v192 offset:39936
	s_mov_b32 m0, s58
	s_add_u32 s44, s34, 0x18000
	s_addc_u32 s45, s35, 0
	global_load_lds_dwordx4 v192, s[44:45] sc1
	v_rcp_f32_e32 v215, v215
	v_mfma_f32_32x32x16_f16 v[96:111], a[64:67], v[160:163], v[96:111]
	ds_read_b128 v[160:163], v192 offset:40960
	v_exp_f32_e32 v200, v144
	v_mfma_f32_32x32x16_f16 v[112:127], a[64:67], v[164:167], v[112:127]
	ds_read_b128 v[164:167], v192 offset:41984
	v_exp_f32_e32 v201, v145
	v_add_f32_e32 v200, 1.0, v200
	v_mfma_f32_32x32x16_f16 v[96:111], a[68:71], v[168:171], v[96:111]
	ds_read_b128 v[168:171], v192 offset:43008
	v_exp_f32_e32 v202, v146
	v_add_f32_e32 v201, 1.0, v201
	v_mfma_f32_32x32x16_f16 v[112:127], a[68:71], v[172:175], v[112:127]
	ds_read_b128 v[172:175], v192 offset:44032
	global_load_lds_dwordx4 v192, s[44:45] offset:1024 sc1
	v_exp_f32_e32 v203, v147
	v_add_f32_e32 v202, 1.0, v202
	s_waitcnt lgkmcnt(2)
	v_mfma_f32_32x32x16_f16 v[96:111], a[72:75], v[176:179], v[96:111]
	ds_read_b128 v[176:179], v192 offset:45056
	v_add_f32_e32 v203, 1.0, v203
	v_rcp_f32_e32 v200, v200
	v_mfma_f32_32x32x16_f16 v[112:127], a[72:75], v[180:183], v[112:127]
	ds_read_b128 v[180:183], v192 offset:46080
	v_rcp_f32_e32 v201, v201
	v_fma_f32 v200, v200, 2.0, -1.0
	v_mfma_f32_32x32x16_f16 v[96:111], a[76:79], v[184:187], v[96:111]
	ds_read_b128 v[184:187], v192 offset:47104
	v_rcp_f32_e32 v202, v202
	v_fma_f32 v201, v201, 2.0, -1.0
	v_mul_f32_e32 v216, v212, v200
	v_mfma_f32_32x32x16_f16 v[112:127], a[76:79], v[188:191], v[112:127]
	ds_read_b128 v[188:191], v192 offset:48128
	global_load_lds_dwordx4 v192, s[44:45] offset:2048 sc1
	v_rcp_f32_e32 v203, v203
	v_fma_f32 v202, v202, 2.0, -1.0
	v_mul_f32_e32 v217, v213, v201
	v_mfma_f32_32x32x16_f16 v[96:111], a[80:83], v[160:163], v[96:111]
	ds_read_b128 v[160:163], v192 offset:49152
	v_fma_f32 v203, v203, 2.0, -1.0
	v_mul_f32_e32 v218, v214, v202
	v_exp_f32_e32 v200, v80
	v_mfma_f32_32x32x16_f16 v[112:127], a[80:83], v[164:167], v[112:127]
	ds_read_b128 v[164:167], v192 offset:50176
	v_mul_f32_e32 v219, v215, v203
	v_mul_f32_e32 v236, v216, v228
	v_exp_f32_e32 v201, v81
	s_waitcnt lgkmcnt(2)
	v_mfma_f32_32x32x16_f16 v[96:111], a[84:87], v[168:171], v[96:111]
	ds_read_b128 v[168:171], v192 offset:51200
	v_mul_f32_e32 v237, v216, v232
	v_fmac_f32_e32 v236, v217, v229
	v_exp_f32_e32 v202, v82
	v_mfma_f32_32x32x16_f16 v[112:127], a[84:87], v[172:175], v[112:127]
	ds_read_b128 v[172:175], v192 offset:52224
	global_load_lds_dwordx4 v192, s[44:45] offset:3072 sc1
	v_fmac_f32_e32 v237, v217, v233
	v_fmac_f32_e32 v236, v218, v230
	v_exp_f32_e32 v203, v83
	v_mfma_f32_32x32x16_f16 v[96:111], a[88:91], v[176:179], v[96:111]
	ds_read_b128 v[176:179], v192 offset:53248
	v_fmac_f32_e32 v237, v218, v234
	v_fmac_f32_e32 v236, v219, v231
	v_exp_f32_e32 v204, v84
	v_mfma_f32_32x32x16_f16 v[112:127], a[88:91], v[180:183], v[112:127]
	ds_read_b128 v[180:183], v192 offset:54272
	v_fmac_f32_e32 v237, v219, v235
	v_mov_b32_e32 v238, v236
	v_exp_f32_e32 v205, v85
	v_mfma_f32_32x32x16_f16 v[96:111], a[92:95], v[184:187], v[96:111]
	ds_read_b128 v[184:187], v192 offset:55296
	v_mov_b32_e32 v240, v237
	v_cvt_pk_f16_f32 v220, v216, v217
	v_exp_f32_e32 v206, v86
	v_mfma_f32_32x32x16_f16 v[112:127], a[92:95], v[188:191], v[112:127]
	ds_read_b128 v[188:191], v192 offset:56320
	s_mov_b32 m0, s59
	s_add_u32 s44, s34, 0x19000
	s_addc_u32 s45, s35, 0
	global_load_lds_dwordx4 v192, s[44:45] sc1
	v_permlane32_swap_b32_e32 v236, v238
	v_permlane32_swap_b32_e32 v237, v240
	v_add_f32_e32 v238, v236, v238
	v_add_f32_e32 v239, v237, v240
	ds_write_b64 v248, v[238:239] offset:1024
	v_exp_f32_e32 v207, v87
	s_waitcnt lgkmcnt(3)
	v_mfma_f32_32x32x16_f16 v[96:111], a[96:99], v[160:163], v[96:111]
	ds_read_b128 v[160:163], v192 offset:57344
	v_cvt_pk_f16_f32 v221, v218, v219
	v_exp_f32_e32 v208, v88
	v_add_f32_e32 v200, 1.0, v200
	v_mfma_f32_32x32x16_f16 v[112:127], a[96:99], v[164:167], v[112:127]
	ds_read_b128 v[164:167], v192 offset:58368
	v_exp_f32_e32 v209, v89
	v_add_f32_e32 v201, 1.0, v201
	v_add_f32_e32 v202, 1.0, v202
	v_mfma_f32_32x32x16_f16 v[96:111], a[100:103], v[168:171], v[96:111]
	ds_read_b128 v[168:171], v192 offset:59392
	v_exp_f32_e32 v210, v90
	v_add_f32_e32 v203, 1.0, v203
	v_add_f32_e32 v204, 1.0, v204
	v_mfma_f32_32x32x16_f16 v[112:127], a[100:103], v[172:175], v[112:127]
	ds_read_b128 v[172:175], v192 offset:60416
	global_load_lds_dwordx4 v192, s[44:45] offset:1024 sc1
	v_exp_f32_e32 v211, v91
	v_add_f32_e32 v205, 1.0, v205
	v_add_f32_e32 v206, 1.0, v206
	v_mfma_f32_32x32x16_f16 v[96:111], a[104:107], v[176:179], v[96:111]
	ds_read_b128 v[176:179], v192 offset:61440
	v_exp_f32_e32 v212, v92
	v_add_f32_e32 v207, 1.0, v207
	v_add_f32_e32 v208, 1.0, v208
	v_mfma_f32_32x32x16_f16 v[112:127], a[104:107], v[180:183], v[112:127]
	ds_read_b128 v[180:183], v192 offset:62464
	v_exp_f32_e32 v213, v93
	v_add_f32_e32 v209, 1.0, v209
	v_add_f32_e32 v210, 1.0, v210
	s_waitcnt lgkmcnt(2)
	v_mfma_f32_32x32x16_f16 v[96:111], a[108:111], v[184:187], v[96:111]
	ds_read_b128 v[184:187], v192 offset:63488
	v_exp_f32_e32 v214, v94
	v_add_f32_e32 v211, 1.0, v211
	v_add_f32_e32 v212, 1.0, v212
	v_mfma_f32_32x32x16_f16 v[112:127], a[108:111], v[188:191], v[112:127]
	ds_read_b128 v[188:191], v192 offset:64512
	global_load_lds_dwordx4 v192, s[44:45] offset:2048 sc1
	v_exp_f32_e32 v215, v95
	v_add_f32_e32 v213, 1.0, v213
	v_add_f32_e32 v214, 1.0, v214
	s_waitcnt vmcnt(7)
	s_barrier
	v_mfma_f32_32x32x16_f16 v[96:111], a[112:115], v[160:163], v[96:111]
	ds_read_b128 v[160:163], v193 offset:0
	v_add_f32_e32 v215, 1.0, v215
	v_rcp_f32_e32 v200, v200
	v_mfma_f32_32x32x16_f16 v[112:127], a[112:115], v[164:167], v[112:127]
	ds_read_b128 v[164:167], v193 offset:1024
	v_rcp_f32_e32 v201, v201
	v_mfma_f32_32x32x16_f16 v[96:111], a[116:119], v[168:171], v[96:111]
	ds_read_b128 v[168:171], v193 offset:2048
	v_rcp_f32_e32 v202, v202
	v_mfma_f32_32x32x16_f16 v[112:127], a[116:119], v[172:175], v[112:127]
	ds_read_b128 v[172:175], v193 offset:3072
	global_load_lds_dwordx4 v192, s[44:45] offset:3072 sc1
	v_rcp_f32_e32 v203, v203
	s_waitcnt lgkmcnt(2)
	v_mfma_f32_32x32x16_f16 v[96:111], a[120:123], v[176:179], v[96:111]
	ds_read_b128 v[176:179], v193 offset:4096
	v_rcp_f32_e32 v204, v204
	v_mfma_f32_32x32x16_f16 v[112:127], a[120:123], v[180:183], v[112:127]
	ds_read_b128 v[180:183], v193 offset:5120
	v_rcp_f32_e32 v205, v205
	v_mul_f32_e32 v204, v204, v148
	v_mfma_f32_32x32x16_f16 v[96:111], a[124:127], v[184:187], v[96:111]
	ds_read_b128 v[184:187], v193 offset:6144
	v_rcp_f32_e32 v206, v206
	v_mul_f32_e32 v205, v205, v149
	v_mfma_f32_32x32x16_f16 v[112:127], a[124:127], v[188:191], v[112:127]
	ds_read_b128 v[188:191], v193 offset:7168
	v_cmp_gt_u32_e32 vcc, 1, v251
	s_cbranch_vccnz .LD_tpoll35
.LD_tok34:
	s_and_b32 s64, s33, 1
	s_lshl_b32 s64, s64, 22
	s_add_u32 s64, s64, s49
	s_add_u32 s34, s6, s64
	s_addc_u32 s35, s7, 0
	s_mov_b32 m0, s52
	s_add_u32 s44, s34, 0x0
	s_addc_u32 s45, s35, 0
	global_load_lds_dwordx4 v192, s[44:45] sc1
	v_rcp_f32_e32 v207, v207
	v_mul_f32_e32 v206, v206, v150
	v_mfma_f32_32x32x16_f16 v[96:111], a[128:131], v[160:163], v[96:111]
	ds_read_b128 v[160:163], v193 offset:8192
	v_rcp_f32_e32 v208, v208
	v_mul_f32_e32 v207, v207, v151
	v_mfma_f32_32x32x16_f16 v[112:127], a[128:131], v[164:167], v[112:127]
	ds_read_b128 v[164:167], v193 offset:9216
	v_rcp_f32_e32 v209, v209
	v_fmamk_f32 v208, v208, 0xc0b8aa3b, v198
	s_waitcnt lgkmcnt(2)
	v_mfma_f32_32x32x16_f16 v[96:111], a[132:135], v[168:171], v[96:111]
	ds_read_b128 v[168:171], v193 offset:10240
	v_rcp_f32_e32 v210, v210
	v_fmamk_f32 v209, v209, 0xc0b8aa3b, v198
	v_fma_f32 v148, v200, v208, v204
	s_add_u32 s46, s42, 0x2000
	s_addc_u32 s47, s43, 0
	global_load_dwordx4 v[32:35], v192, s[46:47] offset:0
	v_mfma_f32_32x32x16_f16 v[112:127], a[132:135], v[172:175], v[112:127]
	ds_read_b128 v[172:175], v193 offset:11264
	global_load_lds_dwordx4 v192, s[44:45] offset:1024 sc1
	v_rcp_f32_e32 v211, v211
	v_fmamk_f32 v210, v210, 0xc0b8aa3b, v198
	v_fma_f32 v149, v201, v209, v205
	global_load_dwordx4 v[36:39], v192, s[46:47] offset:1024
	global_load_dwordx4 v[40:43], v192, s[46:47] offset:2048
	v_mfma_f32_32x32x16_f16 v[96:111], a[136:139], v[176:179], v[96:111]
	ds_read_b128 v[176:179], v193 offset:12288
	v_rcp_f32_e32 v212, v212
	v_fmamk_f32 v211, v211, 0xc0b8aa3b, v198
	v_fma_f32 v150, v202, v210, v206
	global_load_dwordx4 v[44:47], v192, s[46:47] offset:3072
	s_add_u32 s46, s42, 0x3000
	s_addc_u32 s47, s43, 0
	v_mfma_f32_32x32x16_f16 v[112:127], a[136:139], v[180:183], v[112:127]
	ds_read_b128 v[180:183], v193 offset:13312
	v_rcp_f32_e32 v213, v213
	v_fma_f32 v151, v203, v211, v207
	global_load_dwordx4 v[48:51], v192, s[46:47] offset:0
	global_load_dwordx4 v[52:55], v192, s[46:47] offset:1024
	v_mfma_f32_32x32x16_f16 v[96:111], a[140:143], v[184:187], v[96:111]
	ds_read_b128 v[184:187], v193 offset:14336
	v_rcp_f32_e32 v214, v214
	global_load_dwordx4 v[56:59], v192, s[46:47] offset:2048
	global_load_dwordx4 v[60:63], v192, s[46:47] offset:3072
	v_mfma_f32_32x32x16_f16 v[112:127], a[140:143], v[188:191], v[112:127]
	ds_read_b128 v[188:191], v193 offset:15360
	global_load_lds_dwordx4 v192, s[44:45] offset:2048 sc1
	v_rcp_f32_e32 v215, v215
	s_waitcnt lgkmcnt(2)
	v_mfma_f32_32x32x16_f16 v[96:111], a[144:147], v[160:163], v[96:111]
	ds_read_b128 v[160:163], v193 offset:16384
	v_exp_f32_e32 v200, v148
	v_mfma_f32_32x32x16_f16 v[112:127], a[144:147], v[164:167], v[112:127]
	ds_read_b128 v[164:167], v193 offset:17408
	v_exp_f32_e32 v201, v149
	v_add_f32_e32 v200, 1.0, v200
	v_mfma_f32_32x32x16_f16 v[96:111], a[148:151], v[168:171], v[96:111]
	ds_read_b128 v[168:171], v193 offset:18432
	v_exp_f32_e32 v202, v150
	v_add_f32_e32 v201, 1.0, v201
	v_mfma_f32_32x32x16_f16 v[112:127], a[148:151], v[172:175], v[112:127]
	ds_read_b128 v[172:175], v193 offset:19456
	global_load_lds_dwordx4 v192, s[44:45] offset:3072 sc1
	v_exp_f32_e32 v203, v151
	v_add_f32_e32 v202, 1.0, v202
	v_mfma_f32_32x32x16_f16 v[96:111], a[152:155], v[176:179], v[96:111]
	ds_read_b128 v[176:179], v193 offset:20480
	v_add_f32_e32 v203, 1.0, v203
	v_rcp_f32_e32 v200, v200
	v_mfma_f32_32x32x16_f16 v[112:127], a[152:155], v[180:183], v[112:127]
	ds_read_b128 v[180:183], v193 offset:21504
	v_rcp_f32_e32 v201, v201
	v_fma_f32 v200, v200, 2.0, -1.0
	s_waitcnt lgkmcnt(2)
	v_mfma_f32_32x32x16_f16 v[96:111], a[156:159], v[184:187], v[96:111]
	ds_read_b128 v[184:187], v193 offset:22528
	v_rcp_f32_e32 v202, v202
	v_fma_f32 v201, v201, 2.0, -1.0
	v_mul_f32_e32 v216, v212, v200
	v_mfma_f32_32x32x16_f16 v[112:127], a[156:159], v[188:191], v[112:127]
	ds_read_b128 v[188:191], v193 offset:23552
	s_mov_b32 m0, s53
	s_add_u32 s44, s34, 0x1000
	s_addc_u32 s45, s35, 0
	global_load_lds_dwordx4 v192, s[44:45] sc1
	v_rcp_f32_e32 v203, v203
	v_fma_f32 v202, v202, 2.0, -1.0
	v_mul_f32_e32 v217, v213, v201
	v_mfma_f32_32x32x16_f16 v[96:111], a[160:163], v[160:163], v[96:111]
	ds_read_b128 v[160:163], v193 offset:24576
	v_fma_f32 v203, v203, 2.0, -1.0
	v_mul_f32_e32 v218, v214, v202
	v_mfma_f32_32x32x16_f16 v[112:127], a[160:163], v[164:167], v[112:127]
	ds_read_b128 v[164:167], v193 offset:25600
	v_mul_f32_e32 v219, v215, v203
	v_mul_f32_e32 v236, v216, v228
	v_mfma_f32_32x32x16_f16 v[96:111], a[164:167], v[168:171], v[96:111]
	ds_read_b128 v[168:171], v193 offset:26624
	v_mul_f32_e32 v237, v216, v232
	v_fmac_f32_e32 v236, v217, v229
	v_mfma_f32_32x32x16_f16 v[112:127], a[164:167], v[172:175], v[112:127]
	ds_read_b128 v[172:175], v193 offset:27648
	global_load_lds_dwordx4 v192, s[44:45] offset:1024 sc1
	v_fmac_f32_e32 v237, v217, v233
	v_fmac_f32_e32 v236, v218, v230
	s_waitcnt lgkmcnt(2)
	v_mfma_f32_32x32x16_f16 v[96:111], a[168:171], v[176:179], v[96:111]
	ds_read_b128 v[176:179], v193 offset:28672
	v_fmac_f32_e32 v237, v218, v234
	v_fmac_f32_e32 v236, v219, v231
	v_mfma_f32_32x32x16_f16 v[112:127], a[168:171], v[180:183], v[112:127]
	ds_read_b128 v[180:183], v193 offset:29696
	v_fmac_f32_e32 v237, v219, v235
	v_mov_b32_e32 v238, v236
	v_mfma_f32_32x32x16_f16 v[96:111], a[172:175], v[184:187], v[96:111]
	ds_read_b128 v[184:187], v193 offset:30720
	v_mov_b32_e32 v240, v237
	v_cvt_pk_f16_f32 v222, v216, v217
	v_mfma_f32_32x32x16_f16 v[112:127], a[172:175], v[188:191], v[112:127]
	ds_read_b128 v[188:191], v193 offset:31744
	global_load_lds_dwordx4 v192, s[44:45] offset:2048 sc1
	v_permlane32_swap_b32_e32 v236, v238
	v_permlane32_swap_b32_e32 v237, v240
	v_add_f32_e32 v238, v236, v238
	v_add_f32_e32 v239, v237, v240
	ds_write_b64 v248, v[238:239] offset:1280
	s_waitcnt vmcnt(15)
	s_barrier
	v_mfma_f32_32x32x16_f16 v[96:111], a[176:179], v[160:163], v[96:111]
	ds_read_b128 v[160:163], v193 offset:32768
	v_cvt_pk_f16_f32 v223, v218, v219
	v_mfma_f32_32x32x16_f16 v[112:127], a[176:179], v[164:167], v[112:127]
	ds_read_b128 v[164:167], v193 offset:33792
	v_permlane32_swap_b32_e32 v220, v222
	v_permlane32_swap_b32_e32 v221, v223
	s_cmp_eq_u32 s31, 0
	s_cbranch_scc1 .LD_slow36
	global_store_dwordx4 v195, v[220:223], s[36:37] offset:0
